# back-edge rotation (7.11) of the four GEMM K loops: pointer updates, next-tile pointer selects and exit test moved in front of the iteration's last barrier
# baseline (speedup 1.0000x reference)
.LBB0_280:
	s_ashr_i32 s51, s50, 31
	s_lshl_b64 s[6:7], s[50:51], 18
	s_add_u32 s52, s20, s6
	s_addc_u32 s53, s21, s7
	s_and_b64 s[6:7], s[38:39], exec
	s_cselect_b32 s14, s53, s5
	s_cselect_b32 s15, s52, s4
	s_ashr_i32 s49, s48, 31
	s_lshl_b64 s[6:7], s[48:49], 18
	s_add_u32 s54, s34, s6
	s_addc_u32 s55, s35, s7
	s_and_b64 s[6:7], s[38:39], exec
	s_cselect_b32 s16, s55, s3
	s_cselect_b32 s17, s54, s2
	s_add_u32 s30, s2, 0x100
	s_addc_u32 s41, s3, 0
	s_add_u32 s2, s4, 0x20080
	v_mov_b32_e32 v0, 0
	s_addc_u32 s3, s5, 0
	s_mov_b32 s49, -2
	v_mov_b32_e32 v1, v0
	v_mov_b32_e32 v2, v0
	v_mov_b32_e32 v3, v0
	s_waitcnt vmcnt(0)
	v_mov_b32_e32 v20, v0
	v_mov_b32_e32 v21, v0
	v_mov_b32_e32 v22, v0
	v_mov_b32_e32 v23, v0
	v_mov_b32_e32 v24, v0
	v_mov_b32_e32 v25, v0
	v_mov_b32_e32 v26, v0
	v_mov_b32_e32 v27, v0
	v_mov_b32_e32 v28, v0
	v_mov_b32_e32 v29, v0
	v_mov_b32_e32 v30, v0
	v_mov_b32_e32 v31, v0
	v_mov_b32_e32 v40, v0
	v_mov_b32_e32 v41, v0
	v_mov_b32_e32 v42, v0
	v_mov_b32_e32 v43, v0
	v_mov_b32_e32 v44, v0
	v_mov_b32_e32 v45, v0
	v_mov_b32_e32 v46, v0
	v_mov_b32_e32 v47, v0
	v_mov_b32_e32 v56, v0
	v_mov_b32_e32 v57, v0
	v_mov_b32_e32 v58, v0
	v_mov_b32_e32 v59, v0
	v_mov_b32_e32 v60, v0
	v_mov_b32_e32 v61, v0
	v_mov_b32_e32 v62, v0
	v_mov_b32_e32 v63, v0
	v_mov_b32_e32 v32, v0
	v_mov_b32_e32 v33, v0
	v_mov_b32_e32 v34, v0
	v_mov_b32_e32 v35, v0
	v_mov_b32_e32 v36, v0
	v_mov_b32_e32 v37, v0
	v_mov_b32_e32 v38, v0
	v_mov_b32_e32 v39, v0
	v_mov_b32_e32 v48, v0
	v_mov_b32_e32 v49, v0
	v_mov_b32_e32 v50, v0
	v_mov_b32_e32 v51, v0
	v_mov_b32_e32 v52, v0
	v_mov_b32_e32 v53, v0
	v_mov_b32_e32 v54, v0
	v_mov_b32_e32 v55, v0
	v_mov_b32_e32 v64, v0
	v_mov_b32_e32 v65, v0
	v_mov_b32_e32 v66, v0
	v_mov_b32_e32 v67, v0
	v_mov_b32_e32 v68, v0
	v_mov_b32_e32 v69, v0
	v_mov_b32_e32 v70, v0
	v_mov_b32_e32 v71, v0
	v_mov_b32_e32 v72, v0
	v_mov_b32_e32 v73, v0
	v_mov_b32_e32 v74, v0
	v_mov_b32_e32 v75, v0
	v_mov_b32_e32 v76, v0
	v_mov_b32_e32 v77, v0
	v_mov_b32_e32 v78, v0
	v_mov_b32_e32 v79, v0
	v_mov_b32_e32 v80, v0
	v_mov_b32_e32 v81, v0
	v_mov_b32_e32 v82, v0
	v_mov_b32_e32 v83, v0
	v_mov_b32_e32 v84, v0
	v_mov_b32_e32 v85, v0
	v_mov_b32_e32 v86, v0
	v_mov_b32_e32 v87, v0
	v_mov_b32_e32 v88, v0
	v_mov_b32_e32 v89, v0
	v_mov_b32_e32 v90, v0
	v_mov_b32_e32 v91, v0
	v_mov_b32_e32 v92, v0
	v_mov_b32_e32 v93, v0
	v_mov_b32_e32 v94, v0
	v_mov_b32_e32 v95, v0
	v_mov_b32_e32 v104, v0
	v_mov_b32_e32 v105, v0
	v_mov_b32_e32 v106, v0
	v_mov_b32_e32 v107, v0
	v_mov_b32_e32 v108, v0
	v_mov_b32_e32 v109, v0
	v_mov_b32_e32 v110, v0
	v_mov_b32_e32 v111, v0
	v_mov_b32_e32 v120, v0
	v_mov_b32_e32 v121, v0
	v_mov_b32_e32 v122, v0
	v_mov_b32_e32 v123, v0
	v_mov_b32_e32 v124, v0
	v_mov_b32_e32 v125, v0
	v_mov_b32_e32 v126, v0
	v_mov_b32_e32 v127, v0
	v_mov_b32_e32 v96, v0
	v_mov_b32_e32 v97, v0
	v_mov_b32_e32 v98, v0
	v_mov_b32_e32 v99, v0
	v_mov_b32_e32 v100, v0
	v_mov_b32_e32 v101, v0
	v_mov_b32_e32 v102, v0
	v_mov_b32_e32 v103, v0
	v_mov_b32_e32 v112, v0
	v_mov_b32_e32 v113, v0
	v_mov_b32_e32 v114, v0
	v_mov_b32_e32 v115, v0
	v_mov_b32_e32 v116, v0
	v_mov_b32_e32 v117, v0
	v_mov_b32_e32 v118, v0
	v_mov_b32_e32 v119, v0
	v_mov_b32_e32 v128, v0
	v_mov_b32_e32 v129, v0
	v_mov_b32_e32 v130, v0
	v_mov_b32_e32 v131, v0
	v_mov_b32_e32 v132, v0
	v_mov_b32_e32 v133, v0
	v_mov_b32_e32 v134, v0
	v_mov_b32_e32 v135, v0
	v_mov_b32_e32 v136, v0
	v_mov_b32_e32 v137, v0
	v_mov_b32_e32 v138, v0
	v_mov_b32_e32 v139, v0
	v_mov_b32_e32 v140, v0
	v_mov_b32_e32 v141, v0
	v_mov_b32_e32 v142, v0
	v_mov_b32_e32 v143, v0
	s_add_u32 s4, s2, 0xfffe0080
	s_addc_u32 s5, s3, -1
	s_cmp_eq_u32 s49, 4
	s_cselect_b32 s7, s14, s5
	s_cselect_b32 s6, s15, s4
	s_cselect_b32 s5, s16, s41
	s_cselect_b32 s4, s17, s30
.LBB0_281:
	s_add_i32 s51, 0, 0x10000
	s_add_i32 s66, 0, 0x14000
	v_add_u32_e32 v16, s51, v200
	v_add_u32_e32 v167, s66, v200
	ds_read_b128 v[4:7], v16
	ds_read_b128 v[8:11], v16 offset:1024
	ds_read_b128 v[12:15], v16 offset:2048
	ds_read_b128 v[16:19], v16 offset:3072
	ds_read_b128 v[168:171], v167
	ds_read_b128 v[172:175], v167 offset:1024
	ds_read_b128 v[180:183], v167 offset:2048
	ds_read_b128 v[184:187], v167 offset:3072
	v_lshl_add_u64 v[176:177], s[2:3], 0, v[164:165]
	s_add_i32 m0, s37, 0xc000
	ds_read_b128 v[188:191], v206
	ds_read_b128 v[192:195], v206 offset:1024
	ds_read_b128 v[208:211], v206 offset:2048
	ds_read_b128 v[212:215], v206 offset:3072
	ds_read_b128 v[216:219], v206 offset:4096
	ds_read_b128 v[220:223], v206 offset:5120
	ds_read_b128 v[224:227], v206 offset:6144
	ds_read_b128 v[228:231], v206 offset:7168
	global_load_lds_dwordx4 v[176:177], off
	v_lshl_add_u64 v[176:177], s[2:3], 0, v[162:163]
	s_add_i32 m0, s37, 0xe000
	s_nop 0
	global_load_lds_dwordx4 v[176:177], off
	s_waitcnt vmcnt(8)
	s_waitcnt lgkmcnt(0)
	s_barrier
	s_setprio 1
	s_waitcnt lgkmcnt(0)
	v_mfma_i32_16x16x64_i8 v[140:143], v[4:7], v[188:191], v[140:143]
	v_mfma_i32_16x16x64_i8 v[136:139], v[12:15], v[188:191], v[136:139]
	v_mfma_i32_16x16x64_i8 v[132:135], v[4:7], v[208:211], v[132:135]
	v_mfma_i32_16x16x64_i8 v[128:131], v[12:15], v[208:211], v[128:131]
	v_mfma_i32_16x16x64_i8 v[116:119], v[4:7], v[216:219], v[116:119]
	v_mfma_i32_16x16x64_i8 v[112:115], v[12:15], v[216:219], v[112:115]
	v_mfma_i32_16x16x64_i8 v[100:103], v[4:7], v[224:227], v[100:103]
	v_mfma_i32_16x16x64_i8 v[96:99], v[12:15], v[224:227], v[96:99]
	v_mfma_i32_16x16x64_i8 v[140:143], v[8:11], v[192:195], v[140:143]
	v_mfma_i32_16x16x64_i8 v[136:139], v[16:19], v[192:195], v[136:139]
	v_mfma_i32_16x16x64_i8 v[132:135], v[8:11], v[212:215], v[132:135]
	v_mfma_i32_16x16x64_i8 v[128:131], v[16:19], v[212:215], v[128:131]
	v_mfma_i32_16x16x64_i8 v[116:119], v[8:11], v[220:223], v[116:119]
	v_mfma_i32_16x16x64_i8 v[112:115], v[16:19], v[220:223], v[112:115]
	v_mfma_i32_16x16x64_i8 v[100:103], v[8:11], v[228:231], v[100:103]
	v_mfma_i32_16x16x64_i8 v[96:99], v[16:19], v[228:231], v[96:99]
	s_setprio 0
	s_setprio 1
	v_mfma_i32_16x16x64_i8 v[124:127], v[168:171], v[188:191], v[124:127]
	v_mfma_i32_16x16x64_i8 v[120:123], v[180:183], v[188:191], v[120:123]
	v_mfma_i32_16x16x64_i8 v[108:111], v[168:171], v[208:211], v[108:111]
	v_mfma_i32_16x16x64_i8 v[104:107], v[180:183], v[208:211], v[104:107]
	v_mfma_i32_16x16x64_i8 v[92:95], v[168:171], v[216:219], v[92:95]
	v_mfma_i32_16x16x64_i8 v[88:91], v[180:183], v[216:219], v[88:91]
	v_mfma_i32_16x16x64_i8 v[84:87], v[168:171], v[224:227], v[84:87]
	v_mfma_i32_16x16x64_i8 v[80:83], v[180:183], v[224:227], v[80:83]
	v_mfma_i32_16x16x64_i8 v[124:127], v[172:175], v[192:195], v[124:127]
	v_mfma_i32_16x16x64_i8 v[120:123], v[184:187], v[192:195], v[120:123]
	v_mfma_i32_16x16x64_i8 v[108:111], v[172:175], v[212:215], v[108:111]
	v_mfma_i32_16x16x64_i8 v[104:107], v[184:187], v[212:215], v[104:107]
	v_mfma_i32_16x16x64_i8 v[92:95], v[172:175], v[220:223], v[92:95]
	v_mfma_i32_16x16x64_i8 v[88:91], v[184:187], v[220:223], v[88:91]
	v_mfma_i32_16x16x64_i8 v[84:87], v[172:175], v[228:231], v[84:87]
	v_mfma_i32_16x16x64_i8 v[80:83], v[184:187], v[228:231], v[80:83]
	s_setprio 0
	s_barrier
	s_add_i32 s51, s51, s36
	v_lshl_add_u64 v[176:177], s[4:5], 0, v[146:147]
	s_mov_b32 m0, s51
	ds_read_b128 v[188:191], v206 offset:16384
	ds_read_b128 v[192:195], v206 offset:17408
	ds_read_b128 v[208:211], v206 offset:18432
	ds_read_b128 v[212:215], v206 offset:19456
	ds_read_b128 v[216:219], v206 offset:20480
	ds_read_b128 v[220:223], v206 offset:21504
	ds_read_b128 v[224:227], v206 offset:22528
	ds_read_b128 v[228:231], v206 offset:23552
	global_load_lds_dwordx4 v[176:177], off
	s_add_i32 m0, s51, 0x2000
	s_add_u32 s64, s4, 0x20000
	v_lshl_add_u64 v[178:179], s[4:5], 0, v[148:149]
	s_addc_u32 s65, s5, 0
	s_add_i32 s51, s66, s36
	global_load_lds_dwordx4 v[178:179], off
	v_lshl_add_u64 v[196:197], s[64:65], 0, v[146:147]
	s_mov_b32 m0, s51
	v_lshl_add_u64 v[232:233], s[6:7], 0, v[148:149]
	global_load_lds_dwordx4 v[196:197], off
	v_lshl_add_u64 v[196:197], s[64:65], 0, v[148:149]
	s_add_i32 m0, s51, 0x2000
	s_nop 0
	global_load_lds_dwordx4 v[196:197], off
	v_lshl_add_u64 v[196:197], s[6:7], 0, v[146:147]
	s_mov_b32 m0, s37
	s_nop 0
	global_load_lds_dwordx4 v[196:197], off
	s_mov_b32 m0, s57
	s_nop 0
	global_load_lds_dwordx4 v[232:233], off
	s_waitcnt vmcnt(8)
	s_waitcnt lgkmcnt(0)
	s_barrier
	s_setprio 1
	s_waitcnt lgkmcnt(0)
	v_mfma_i32_16x16x64_i8 v[76:79], v[4:7], v[188:191], v[76:79]
	v_mfma_i32_16x16x64_i8 v[72:75], v[12:15], v[188:191], v[72:75]
	v_mfma_i32_16x16x64_i8 v[68:71], v[4:7], v[208:211], v[68:71]
	v_mfma_i32_16x16x64_i8 v[64:67], v[12:15], v[208:211], v[64:67]
	v_mfma_i32_16x16x64_i8 v[52:55], v[4:7], v[216:219], v[52:55]
	v_mfma_i32_16x16x64_i8 v[48:51], v[12:15], v[216:219], v[48:51]
	v_mfma_i32_16x16x64_i8 v[4:7], v[4:7], v[224:227], v[36:39]
	v_mfma_i32_16x16x64_i8 v[76:79], v[8:11], v[192:195], v[76:79]
	v_mfma_i32_16x16x64_i8 v[72:75], v[16:19], v[192:195], v[72:75]
	v_mfma_i32_16x16x64_i8 v[68:71], v[8:11], v[212:215], v[68:71]
	v_mfma_i32_16x16x64_i8 v[64:67], v[16:19], v[212:215], v[64:67]
	v_mfma_i32_16x16x64_i8 v[52:55], v[8:11], v[220:223], v[52:55]
	v_mfma_i32_16x16x64_i8 v[48:51], v[16:19], v[220:223], v[48:51]
	v_mfma_i32_16x16x64_i8 v[4:7], v[8:11], v[228:231], v[4:7]
	v_mfma_i32_16x16x64_i8 v[8:11], v[12:15], v[224:227], v[32:35]
	v_mfma_i32_16x16x64_i8 v[8:11], v[16:19], v[228:231], v[8:11]
	s_setprio 0
	s_setprio 1
	v_mfma_i32_16x16x64_i8 v[32:35], v[168:171], v[208:211], v[44:47]
	v_mfma_i32_16x16x64_i8 v[44:47], v[172:175], v[212:215], v[32:35]
	v_mfma_i32_16x16x64_i8 v[32:35], v[180:183], v[208:211], v[40:43]
	v_mfma_i32_16x16x64_i8 v[28:31], v[168:171], v[216:219], v[28:31]
	v_mfma_i32_16x16x64_i8 v[24:27], v[180:183], v[216:219], v[24:27]
	v_mfma_i32_16x16x64_i8 v[20:23], v[168:171], v[224:227], v[20:23]
	v_mfma_i32_16x16x64_i8 v[0:3], v[180:183], v[224:227], v[0:3]
	v_mfma_i32_16x16x64_i8 v[12:15], v[168:171], v[188:191], v[60:63]
	v_mfma_i32_16x16x64_i8 v[16:19], v[180:183], v[188:191], v[56:59]
	v_mfma_i32_16x16x64_i8 v[40:43], v[184:187], v[212:215], v[32:35]
	v_mfma_i32_16x16x64_i8 v[28:31], v[172:175], v[220:223], v[28:31]
	v_mfma_i32_16x16x64_i8 v[24:27], v[184:187], v[220:223], v[24:27]
	v_mfma_i32_16x16x64_i8 v[20:23], v[172:175], v[228:231], v[20:23]
	v_mfma_i32_16x16x64_i8 v[0:3], v[184:187], v[228:231], v[0:3]
	v_mfma_i32_16x16x64_i8 v[12:15], v[172:175], v[192:195], v[12:15]
	v_mfma_i32_16x16x64_i8 v[16:19], v[184:187], v[192:195], v[16:19]
	s_setprio 0
	s_barrier
	s_add_i32 s51, 0, 0x18000
	s_add_i32 s64, 0, 0x1c000
	v_add_u32_e32 v60, s51, v200
	v_add_u32_e32 v167, s64, v200
	ds_read_b128 v[32:35], v60
	ds_read_b128 v[36:39], v60 offset:1024
	ds_read_b128 v[56:59], v60 offset:2048
	ds_read_b128 v[60:63], v60 offset:3072
	ds_read_b128 v[168:171], v167
	ds_read_b128 v[172:175], v167 offset:1024
	ds_read_b128 v[180:183], v167 offset:2048
	ds_read_b128 v[184:187], v167 offset:3072
	s_add_u32 s6, s6, 0x20000
	s_addc_u32 s7, s7, 0
	s_mov_b32 m0, s58
	v_lshl_add_u64 v[234:235], s[6:7], 0, v[146:147]
	ds_read_b128 v[188:191], v206 offset:32768
	ds_read_b128 v[192:195], v206 offset:33792
	ds_read_b128 v[208:211], v206 offset:34816
	ds_read_b128 v[212:215], v206 offset:35840
	ds_read_b128 v[216:219], v206 offset:36864
	ds_read_b128 v[220:223], v206 offset:37888
	ds_read_b128 v[224:227], v206 offset:38912
	ds_read_b128 v[228:231], v206 offset:39936
	global_load_lds_dwordx4 v[234:235], off
	v_lshl_add_u64 v[234:235], s[6:7], 0, v[148:149]
	s_mov_b32 m0, s59
	s_nop 0
	global_load_lds_dwordx4 v[234:235], off
	s_waitcnt vmcnt(8)
	s_waitcnt lgkmcnt(0)
	s_barrier
	s_setprio 1
	s_waitcnt lgkmcnt(0)
	v_mfma_i32_16x16x64_i8 v[140:143], v[32:35], v[188:191], v[140:143]
	v_mfma_i32_16x16x64_i8 v[136:139], v[56:59], v[188:191], v[136:139]
	v_mfma_i32_16x16x64_i8 v[132:135], v[32:35], v[208:211], v[132:135]
	v_mfma_i32_16x16x64_i8 v[128:131], v[56:59], v[208:211], v[128:131]
	v_mfma_i32_16x16x64_i8 v[116:119], v[32:35], v[216:219], v[116:119]
	v_mfma_i32_16x16x64_i8 v[112:115], v[56:59], v[216:219], v[112:115]
	v_mfma_i32_16x16x64_i8 v[100:103], v[32:35], v[224:227], v[100:103]
	v_mfma_i32_16x16x64_i8 v[96:99], v[56:59], v[224:227], v[96:99]
	v_mfma_i32_16x16x64_i8 v[140:143], v[36:39], v[192:195], v[140:143]
	v_mfma_i32_16x16x64_i8 v[136:139], v[60:63], v[192:195], v[136:139]
	v_mfma_i32_16x16x64_i8 v[132:135], v[36:39], v[212:215], v[132:135]
	v_mfma_i32_16x16x64_i8 v[128:131], v[60:63], v[212:215], v[128:131]
	v_mfma_i32_16x16x64_i8 v[116:119], v[36:39], v[220:223], v[116:119]
	v_mfma_i32_16x16x64_i8 v[112:115], v[60:63], v[220:223], v[112:115]
	v_mfma_i32_16x16x64_i8 v[100:103], v[36:39], v[228:231], v[100:103]
	v_mfma_i32_16x16x64_i8 v[96:99], v[60:63], v[228:231], v[96:99]
	s_setprio 0
	s_setprio 1
	v_mfma_i32_16x16x64_i8 v[124:127], v[168:171], v[188:191], v[124:127]
	v_mfma_i32_16x16x64_i8 v[120:123], v[180:183], v[188:191], v[120:123]
	v_mfma_i32_16x16x64_i8 v[108:111], v[168:171], v[208:211], v[108:111]
	v_mfma_i32_16x16x64_i8 v[104:107], v[180:183], v[208:211], v[104:107]
	v_mfma_i32_16x16x64_i8 v[92:95], v[168:171], v[216:219], v[92:95]
	v_mfma_i32_16x16x64_i8 v[88:91], v[180:183], v[216:219], v[88:91]
	v_mfma_i32_16x16x64_i8 v[84:87], v[168:171], v[224:227], v[84:87]
	v_mfma_i32_16x16x64_i8 v[80:83], v[180:183], v[224:227], v[80:83]
	v_mfma_i32_16x16x64_i8 v[124:127], v[172:175], v[192:195], v[124:127]
	v_mfma_i32_16x16x64_i8 v[120:123], v[184:187], v[192:195], v[120:123]
	v_mfma_i32_16x16x64_i8 v[108:111], v[172:175], v[212:215], v[108:111]
	v_mfma_i32_16x16x64_i8 v[104:107], v[184:187], v[212:215], v[104:107]
	v_mfma_i32_16x16x64_i8 v[92:95], v[172:175], v[220:223], v[92:95]
	v_mfma_i32_16x16x64_i8 v[88:91], v[184:187], v[220:223], v[88:91]
	v_mfma_i32_16x16x64_i8 v[84:87], v[172:175], v[228:231], v[84:87]
	v_mfma_i32_16x16x64_i8 v[80:83], v[184:187], v[228:231], v[80:83]
	s_setprio 0
	s_barrier
	s_add_i32 s6, s51, s36
	v_lshl_add_u64 v[176:177], v[176:177], 0, s[8:9]
	s_mov_b32 m0, s6
	ds_read_b128 v[188:191], v206 offset:49152
	ds_read_b128 v[192:195], v206 offset:50176
	ds_read_b128 v[208:211], v206 offset:51200
	ds_read_b128 v[212:215], v206 offset:52224
	ds_read_b128 v[216:219], v206 offset:53248
	ds_read_b128 v[220:223], v206 offset:54272
	ds_read_b128 v[224:227], v206 offset:55296
	ds_read_b128 v[228:231], v206 offset:56320
	global_load_lds_dwordx4 v[176:177], off
	s_add_i32 m0, s6, 0x2000
	s_add_u32 s4, s4, 0x20080
	v_lshl_add_u64 v[176:177], v[178:179], 0, s[8:9]
	s_addc_u32 s5, s5, 0
	s_add_i32 s6, s64, s36
	global_load_lds_dwordx4 v[176:177], off
	v_lshl_add_u64 v[176:177], s[4:5], 0, v[146:147]
	s_mov_b32 m0, s6
	s_nop 0
	global_load_lds_dwordx4 v[176:177], off
	v_lshl_add_u64 v[176:177], s[4:5], 0, v[148:149]
	s_add_i32 m0, s6, 0x2000
	s_nop 0
	global_load_lds_dwordx4 v[176:177], off
	v_lshl_add_u64 v[176:177], v[196:197], 0, s[8:9]
	s_mov_b32 m0, s60
	s_nop 0
	global_load_lds_dwordx4 v[176:177], off
	v_lshl_add_u64 v[176:177], v[232:233], 0, s[8:9]
	s_mov_b32 m0, s61
	s_nop 0
	global_load_lds_dwordx4 v[176:177], off
	s_waitcnt vmcnt(8)
	s_waitcnt lgkmcnt(0)
	s_barrier
	s_setprio 1
	s_waitcnt lgkmcnt(0)
	v_mfma_i32_16x16x64_i8 v[76:79], v[32:35], v[188:191], v[76:79]
	v_mfma_i32_16x16x64_i8 v[68:71], v[32:35], v[208:211], v[68:71]
	v_mfma_i32_16x16x64_i8 v[52:55], v[32:35], v[216:219], v[52:55]
	v_mfma_i32_16x16x64_i8 v[4:7], v[32:35], v[224:227], v[4:7]
	v_mfma_i32_16x16x64_i8 v[76:79], v[36:39], v[192:195], v[76:79]
	v_mfma_i32_16x16x64_i8 v[72:75], v[56:59], v[188:191], v[72:75]
	v_mfma_i32_16x16x64_i8 v[68:71], v[36:39], v[212:215], v[68:71]
	v_mfma_i32_16x16x64_i8 v[64:67], v[56:59], v[208:211], v[64:67]
	v_mfma_i32_16x16x64_i8 v[52:55], v[36:39], v[220:223], v[52:55]
	v_mfma_i32_16x16x64_i8 v[48:51], v[56:59], v[216:219], v[48:51]
	v_mfma_i32_16x16x64_i8 v[36:39], v[36:39], v[228:231], v[4:7]
	v_mfma_i32_16x16x64_i8 v[4:7], v[56:59], v[224:227], v[8:11]
	v_mfma_i32_16x16x64_i8 v[72:75], v[60:63], v[192:195], v[72:75]
	v_mfma_i32_16x16x64_i8 v[64:67], v[60:63], v[212:215], v[64:67]
	v_mfma_i32_16x16x64_i8 v[48:51], v[60:63], v[220:223], v[48:51]
	v_mfma_i32_16x16x64_i8 v[32:35], v[60:63], v[228:231], v[4:7]
	s_setprio 0
	s_setprio 1
	v_mfma_i32_16x16x64_i8 v[4:7], v[168:171], v[188:191], v[12:15]
	v_mfma_i32_16x16x64_i8 v[60:63], v[172:175], v[192:195], v[4:7]
	v_mfma_i32_16x16x64_i8 v[4:7], v[180:183], v[188:191], v[16:19]
	v_mfma_i32_16x16x64_i8 v[56:59], v[184:187], v[192:195], v[4:7]
	v_mfma_i32_16x16x64_i8 v[4:7], v[168:171], v[208:211], v[44:47]
	v_mfma_i32_16x16x64_i8 v[44:47], v[172:175], v[212:215], v[4:7]
	v_mfma_i32_16x16x64_i8 v[4:7], v[180:183], v[208:211], v[40:43]
	v_mfma_i32_16x16x64_i8 v[40:43], v[184:187], v[212:215], v[4:7]
	v_mfma_i32_16x16x64_i8 v[4:7], v[168:171], v[216:219], v[28:31]
	v_mfma_i32_16x16x64_i8 v[28:31], v[172:175], v[220:223], v[4:7]
	v_mfma_i32_16x16x64_i8 v[4:7], v[180:183], v[216:219], v[24:27]
	v_mfma_i32_16x16x64_i8 v[24:27], v[184:187], v[220:223], v[4:7]
	v_mfma_i32_16x16x64_i8 v[4:7], v[168:171], v[224:227], v[20:23]
	v_mfma_i32_16x16x64_i8 v[0:3], v[180:183], v[224:227], v[0:3]
	v_mfma_i32_16x16x64_i8 v[20:23], v[172:175], v[228:231], v[4:7]
	v_mfma_i32_16x16x64_i8 v[0:3], v[184:187], v[228:231], v[0:3]
	s_setprio 0
	s_add_i32 s49, s49, 2
	s_add_u32 s30, s30, 0x100
	s_addc_u32 s41, s41, 0
	s_add_u32 s2, s2, 0x100
	s_addc_u32 s3, s3, 0
	s_add_u32 s4, s2, 0xfffe0080
	s_addc_u32 s5, s3, -1
	s_cmp_eq_u32 s49, 4
	s_cselect_b32 s7, s14, s5
	s_cselect_b32 s6, s15, s4
	s_cselect_b32 s5, s16, s41
	s_cselect_b32 s4, s17, s30
	s_cmp_gt_u32 s49, 5
	s_barrier
	s_cbranch_scc0 .LBB0_281
	s_and_b64 vcc, exec, s[46:47]
	s_cbranch_vccz .LBB0_284
	s_barrier

.LBB0_754:
	s_ashr_i32 s55, s54, 31
	s_lshl_b64 s[4:5], s[54:55], 19
	s_add_u32 s56, s18, s4
	s_addc_u32 s57, s19, s5
	s_and_b64 s[4:5], s[38:39], exec
	s_cselect_b32 s55, s57, s7
	s_cselect_b32 s62, s56, s6
	s_ashr_i32 s53, s52, 31
	s_lshl_b64 s[4:5], s[52:53], 19
	s_add_u32 s58, s20, s4
	s_addc_u32 s59, s21, s5
	s_and_b64 s[4:5], s[38:39], exec
	s_cselect_b32 s53, s59, s3
	s_cselect_b32 s63, s58, s2
	s_add_u32 s70, s2, 0x100
	s_addc_u32 s71, s3, 0
	s_add_u32 s2, s6, 0x40080
	v_mov_b32_e32 v0, 0
	s_addc_u32 s3, s7, 0
	s_mov_b32 s72, -2
	v_mov_b32_e32 v1, v0
	v_mov_b32_e32 v2, v0
	v_mov_b32_e32 v3, v0
	v_mov_b32_e32 v4, v0
	v_mov_b32_e32 v5, v0
	v_mov_b32_e32 v6, v0
	v_mov_b32_e32 v7, v0
	v_mov_b32_e32 v8, v0
	v_mov_b32_e32 v9, v0
	v_mov_b32_e32 v10, v0
	v_mov_b32_e32 v11, v0
	v_mov_b32_e32 v16, v0
	v_mov_b32_e32 v17, v0
	v_mov_b32_e32 v18, v0
	v_mov_b32_e32 v19, v0
	v_mov_b32_e32 v24, v0
	v_mov_b32_e32 v25, v0
	v_mov_b32_e32 v26, v0
	v_mov_b32_e32 v27, v0
	v_mov_b32_e32 v32, v0
	v_mov_b32_e32 v33, v0
	v_mov_b32_e32 v34, v0
	v_mov_b32_e32 v35, v0
	v_mov_b32_e32 v40, v0
	v_mov_b32_e32 v41, v0
	v_mov_b32_e32 v42, v0
	v_mov_b32_e32 v43, v0
	v_mov_b32_e32 v52, v0
	v_mov_b32_e32 v53, v0
	v_mov_b32_e32 v54, v0
	v_mov_b32_e32 v55, v0
	v_mov_b32_e32 v12, v0
	v_mov_b32_e32 v13, v0
	v_mov_b32_e32 v14, v0
	v_mov_b32_e32 v15, v0
	v_mov_b32_e32 v20, v0
	v_mov_b32_e32 v21, v0
	v_mov_b32_e32 v22, v0
	v_mov_b32_e32 v23, v0
	v_mov_b32_e32 v28, v0
	v_mov_b32_e32 v29, v0
	v_mov_b32_e32 v30, v0
	v_mov_b32_e32 v31, v0
	v_mov_b32_e32 v36, v0
	v_mov_b32_e32 v37, v0
	v_mov_b32_e32 v38, v0
	v_mov_b32_e32 v39, v0
	v_mov_b32_e32 v44, v0
	v_mov_b32_e32 v45, v0
	v_mov_b32_e32 v46, v0
	v_mov_b32_e32 v47, v0
	v_mov_b32_e32 v48, v0
	v_mov_b32_e32 v49, v0
	v_mov_b32_e32 v50, v0
	v_mov_b32_e32 v51, v0
	v_mov_b32_e32 v56, v0
	v_mov_b32_e32 v57, v0
	v_mov_b32_e32 v58, v0
	v_mov_b32_e32 v59, v0
	v_mov_b32_e32 v60, v0
	v_mov_b32_e32 v61, v0
	v_mov_b32_e32 v62, v0
	v_mov_b32_e32 v63, v0
	v_mov_b32_e32 v64, v0
	v_mov_b32_e32 v65, v0
	v_mov_b32_e32 v66, v0
	v_mov_b32_e32 v67, v0
	v_mov_b32_e32 v68, v0
	v_mov_b32_e32 v69, v0
	v_mov_b32_e32 v70, v0
	v_mov_b32_e32 v71, v0
	v_mov_b32_e32 v72, v0
	v_mov_b32_e32 v73, v0
	v_mov_b32_e32 v74, v0
	v_mov_b32_e32 v75, v0
	v_mov_b32_e32 v80, v0
	v_mov_b32_e32 v81, v0
	v_mov_b32_e32 v82, v0
	v_mov_b32_e32 v83, v0
	v_mov_b32_e32 v96, v0
	v_mov_b32_e32 v97, v0
	v_mov_b32_e32 v98, v0
	v_mov_b32_e32 v99, v0
	v_mov_b32_e32 v104, v0
	v_mov_b32_e32 v105, v0
	v_mov_b32_e32 v106, v0
	v_mov_b32_e32 v107, v0
	v_mov_b32_e32 v128, v0
	v_mov_b32_e32 v129, v0
	v_mov_b32_e32 v130, v0
	v_mov_b32_e32 v131, v0
	v_mov_b32_e32 v132, v0
	v_mov_b32_e32 v133, v0
	v_mov_b32_e32 v134, v0
	v_mov_b32_e32 v135, v0
	v_mov_b32_e32 v76, v0
	v_mov_b32_e32 v77, v0
	v_mov_b32_e32 v78, v0
	v_mov_b32_e32 v79, v0
	v_mov_b32_e32 v84, v0
	v_mov_b32_e32 v85, v0
	v_mov_b32_e32 v86, v0
	v_mov_b32_e32 v87, v0
	v_mov_b32_e32 v88, v0
	v_mov_b32_e32 v89, v0
	v_mov_b32_e32 v90, v0
	v_mov_b32_e32 v91, v0
	v_mov_b32_e32 v92, v0
	v_mov_b32_e32 v93, v0
	v_mov_b32_e32 v94, v0
	v_mov_b32_e32 v95, v0
	v_mov_b32_e32 v120, v0
	v_mov_b32_e32 v121, v0
	v_mov_b32_e32 v122, v0
	v_mov_b32_e32 v123, v0
	v_mov_b32_e32 v124, v0
	v_mov_b32_e32 v125, v0
	v_mov_b32_e32 v126, v0
	v_mov_b32_e32 v127, v0
	v_mov_b32_e32 v136, v0
	v_mov_b32_e32 v137, v0
	v_mov_b32_e32 v138, v0
	v_mov_b32_e32 v139, v0
	v_mov_b32_e32 v140, v0
	v_mov_b32_e32 v141, v0
	v_mov_b32_e32 v142, v0
	v_mov_b32_e32 v143, v0
	s_add_u32 s4, s2, 0xfffc0080
	s_addc_u32 s5, s3, -1
	s_cmp_eq_u32 s72, 12
	s_cselect_b32 s7, s55, s5
	s_cselect_b32 s6, s62, s4
	s_cselect_b32 s5, s53, s71
	s_cselect_b32 s4, s63, s70
.LBB0_755:
	s_add_i32 s73, 0, 0x10000
	s_add_i32 s76, 0, 0x14000
	v_add_u32_e32 v116, s73, v212
	v_add_u32_e32 v158, s76, v212
	ds_read_b128 v[100:103], v116
	ds_read_b128 v[108:111], v116 offset:1024
	ds_read_b128 v[112:115], v116 offset:2048
	ds_read_b128 v[116:119], v116 offset:3072
	ds_read_b128 v[146:149], v158
	ds_read_b128 v[150:153], v158 offset:1024
	ds_read_b128 v[154:157], v158 offset:2048
	ds_read_b128 v[158:161], v158 offset:3072
	v_lshl_add_u64 v[178:179], s[2:3], 0, v[190:191]
	s_add_i32 m0, s36, 0xc000
	ds_read_b128 v[162:165], v213
	ds_read_b128 v[166:169], v213 offset:1024
	ds_read_b128 v[170:173], v213 offset:2048
	ds_read_b128 v[174:177], v213 offset:3072
	ds_read_b128 v[192:195], v213 offset:4096
	ds_read_b128 v[196:199], v213 offset:5120
	ds_read_b128 v[200:203], v213 offset:6144
	ds_read_b128 v[204:207], v213 offset:7168
	global_load_lds_dwordx4 v[178:179], off
	v_lshl_add_u64 v[178:179], s[2:3], 0, v[188:189]
	s_add_i32 m0, s36, 0xe000
	s_nop 0
	global_load_lds_dwordx4 v[178:179], off
	s_waitcnt vmcnt(8)
	s_waitcnt lgkmcnt(0)
	s_barrier
	s_setprio 1
	s_waitcnt lgkmcnt(0)
	v_mfma_f32_16x16x32_bf16 v[140:143], v[100:103], v[162:165], v[140:143]
	v_mfma_f32_16x16x32_bf16 v[136:139], v[112:115], v[162:165], v[136:139]
	v_mfma_f32_16x16x32_bf16 v[124:127], v[100:103], v[170:173], v[124:127]
	v_mfma_f32_16x16x32_bf16 v[120:123], v[112:115], v[170:173], v[120:123]
	v_mfma_f32_16x16x32_bf16 v[92:95], v[100:103], v[192:195], v[92:95]
	v_mfma_f32_16x16x32_bf16 v[88:91], v[112:115], v[192:195], v[88:91]
	v_mfma_f32_16x16x32_bf16 v[84:87], v[100:103], v[200:203], v[84:87]
	v_mfma_f32_16x16x32_bf16 v[76:79], v[112:115], v[200:203], v[76:79]
	v_mfma_f32_16x16x32_bf16 v[140:143], v[108:111], v[166:169], v[140:143]
	v_mfma_f32_16x16x32_bf16 v[136:139], v[116:119], v[166:169], v[136:139]
	v_mfma_f32_16x16x32_bf16 v[124:127], v[108:111], v[174:177], v[124:127]
	v_mfma_f32_16x16x32_bf16 v[120:123], v[116:119], v[174:177], v[120:123]
	v_mfma_f32_16x16x32_bf16 v[92:95], v[108:111], v[196:199], v[92:95]
	v_mfma_f32_16x16x32_bf16 v[88:91], v[116:119], v[196:199], v[88:91]
	v_mfma_f32_16x16x32_bf16 v[84:87], v[108:111], v[204:207], v[84:87]
	v_mfma_f32_16x16x32_bf16 v[76:79], v[116:119], v[204:207], v[76:79]
	s_setprio 0
	s_setprio 1
	v_mfma_f32_16x16x32_bf16 v[132:135], v[146:149], v[162:165], v[132:135]
	v_mfma_f32_16x16x32_bf16 v[128:131], v[154:157], v[162:165], v[128:131]
	v_mfma_f32_16x16x32_bf16 v[104:107], v[146:149], v[170:173], v[104:107]
	v_mfma_f32_16x16x32_bf16 v[96:99], v[154:157], v[170:173], v[96:99]
	v_mfma_f32_16x16x32_bf16 v[80:83], v[146:149], v[192:195], v[80:83]
	v_mfma_f32_16x16x32_bf16 v[72:75], v[154:157], v[192:195], v[72:75]
	v_mfma_f32_16x16x32_bf16 v[68:71], v[146:149], v[200:203], v[68:71]
	v_mfma_f32_16x16x32_bf16 v[64:67], v[154:157], v[200:203], v[64:67]
	v_mfma_f32_16x16x32_bf16 v[132:135], v[150:153], v[166:169], v[132:135]
	v_mfma_f32_16x16x32_bf16 v[128:131], v[158:161], v[166:169], v[128:131]
	v_mfma_f32_16x16x32_bf16 v[104:107], v[150:153], v[174:177], v[104:107]
	v_mfma_f32_16x16x32_bf16 v[96:99], v[158:161], v[174:177], v[96:99]
	v_mfma_f32_16x16x32_bf16 v[80:83], v[150:153], v[196:199], v[80:83]
	v_mfma_f32_16x16x32_bf16 v[72:75], v[158:161], v[196:199], v[72:75]
	v_mfma_f32_16x16x32_bf16 v[68:71], v[150:153], v[204:207], v[68:71]
	v_mfma_f32_16x16x32_bf16 v[64:67], v[158:161], v[204:207], v[64:67]
	s_setprio 0
	s_barrier
	s_add_i32 s73, s73, s28
	v_lshl_add_u64 v[178:179], s[4:5], 0, v[182:183]
	s_mov_b32 m0, s73
	ds_read_b128 v[162:165], v213 offset:16384
	ds_read_b128 v[166:169], v213 offset:17408
	ds_read_b128 v[170:173], v213 offset:18432
	ds_read_b128 v[174:177], v213 offset:19456
	ds_read_b128 v[192:195], v213 offset:20480
	ds_read_b128 v[196:199], v213 offset:21504
	ds_read_b128 v[200:203], v213 offset:22528
	ds_read_b128 v[204:207], v213 offset:23552
	global_load_lds_dwordx4 v[178:179], off
	s_add_i32 m0, s73, 0x2000
	s_add_u32 s74, s4, 0x40000
	v_lshl_add_u64 v[208:209], s[4:5], 0, v[180:181]
	s_addc_u32 s75, s5, 0
	s_add_i32 s73, s76, s28
	global_load_lds_dwordx4 v[208:209], off
	v_lshl_add_u64 v[210:211], s[74:75], 0, v[182:183]
	s_mov_b32 m0, s73
	v_lshl_add_u64 v[214:215], s[6:7], 0, v[180:181]
	global_load_lds_dwordx4 v[210:211], off
	v_lshl_add_u64 v[210:211], s[74:75], 0, v[180:181]
	s_add_i32 m0, s73, 0x2000
	s_nop 0
	global_load_lds_dwordx4 v[210:211], off
	v_lshl_add_u64 v[210:211], s[6:7], 0, v[182:183]
	s_mov_b32 m0, s36
	s_nop 0
	global_load_lds_dwordx4 v[210:211], off
	s_mov_b32 m0, s37
	s_nop 0
	global_load_lds_dwordx4 v[214:215], off
	s_waitcnt vmcnt(8)
	s_waitcnt lgkmcnt(0)
	s_barrier
	s_setprio 1
	s_waitcnt lgkmcnt(0)
	v_mfma_f32_16x16x32_bf16 v[60:63], v[100:103], v[162:165], v[60:63]
	v_mfma_f32_16x16x32_bf16 v[56:59], v[112:115], v[162:165], v[56:59]
	v_mfma_f32_16x16x32_bf16 v[48:51], v[100:103], v[170:173], v[48:51]
	v_mfma_f32_16x16x32_bf16 v[44:47], v[112:115], v[170:173], v[44:47]
	v_mfma_f32_16x16x32_bf16 v[36:39], v[100:103], v[192:195], v[36:39]
	v_mfma_f32_16x16x32_bf16 v[28:31], v[112:115], v[192:195], v[28:31]
	v_mfma_f32_16x16x32_bf16 v[20:23], v[100:103], v[200:203], v[20:23]
	v_mfma_f32_16x16x32_bf16 v[12:15], v[112:115], v[200:203], v[12:15]
	v_mfma_f32_16x16x32_bf16 v[60:63], v[108:111], v[166:169], v[60:63]
	v_mfma_f32_16x16x32_bf16 v[56:59], v[116:119], v[166:169], v[56:59]
	v_mfma_f32_16x16x32_bf16 v[48:51], v[108:111], v[174:177], v[48:51]
	v_mfma_f32_16x16x32_bf16 v[44:47], v[116:119], v[174:177], v[44:47]
	v_mfma_f32_16x16x32_bf16 v[36:39], v[108:111], v[196:199], v[36:39]
	v_mfma_f32_16x16x32_bf16 v[28:31], v[116:119], v[196:199], v[28:31]
	v_mfma_f32_16x16x32_bf16 v[20:23], v[108:111], v[204:207], v[20:23]
	v_mfma_f32_16x16x32_bf16 v[12:15], v[116:119], v[204:207], v[12:15]
	s_setprio 0
	s_setprio 1
	v_mfma_f32_16x16x32_bf16 v[52:55], v[146:149], v[162:165], v[52:55]
	v_mfma_f32_16x16x32_bf16 v[40:43], v[154:157], v[162:165], v[40:43]
	v_mfma_f32_16x16x32_bf16 v[32:35], v[146:149], v[170:173], v[32:35]
	v_mfma_f32_16x16x32_bf16 v[24:27], v[154:157], v[170:173], v[24:27]
	v_mfma_f32_16x16x32_bf16 v[16:19], v[146:149], v[192:195], v[16:19]
	v_mfma_f32_16x16x32_bf16 v[8:11], v[154:157], v[192:195], v[8:11]
	v_mfma_f32_16x16x32_bf16 v[4:7], v[146:149], v[200:203], v[4:7]
	v_mfma_f32_16x16x32_bf16 v[0:3], v[154:157], v[200:203], v[0:3]
	v_mfma_f32_16x16x32_bf16 v[52:55], v[150:153], v[166:169], v[52:55]
	v_mfma_f32_16x16x32_bf16 v[40:43], v[158:161], v[166:169], v[40:43]
	v_mfma_f32_16x16x32_bf16 v[32:35], v[150:153], v[174:177], v[32:35]
	v_mfma_f32_16x16x32_bf16 v[24:27], v[158:161], v[174:177], v[24:27]
	v_mfma_f32_16x16x32_bf16 v[16:19], v[150:153], v[196:199], v[16:19]
	v_mfma_f32_16x16x32_bf16 v[8:11], v[158:161], v[196:199], v[8:11]
	v_mfma_f32_16x16x32_bf16 v[4:7], v[150:153], v[204:207], v[4:7]
	v_mfma_f32_16x16x32_bf16 v[0:3], v[158:161], v[204:207], v[0:3]
	s_setprio 0
	s_barrier
	s_add_i32 s73, 0, 0x18000
	s_add_i32 s74, 0, 0x1c000
	v_add_u32_e32 v116, s73, v212
	v_add_u32_e32 v158, s74, v212
	ds_read_b128 v[100:103], v116
	ds_read_b128 v[108:111], v116 offset:1024
	ds_read_b128 v[112:115], v116 offset:2048
	ds_read_b128 v[116:119], v116 offset:3072
	ds_read_b128 v[146:149], v158
	ds_read_b128 v[150:153], v158 offset:1024
	ds_read_b128 v[154:157], v158 offset:2048
	ds_read_b128 v[158:161], v158 offset:3072
	s_add_u32 s6, s6, 0x40000
	s_addc_u32 s7, s7, 0
	s_mov_b32 m0, s61
	v_lshl_add_u64 v[216:217], s[6:7], 0, v[182:183]
	ds_read_b128 v[162:165], v213 offset:32768
	ds_read_b128 v[166:169], v213 offset:33792
	ds_read_b128 v[170:173], v213 offset:34816
	ds_read_b128 v[174:177], v213 offset:35840
	ds_read_b128 v[192:195], v213 offset:36864
	ds_read_b128 v[196:199], v213 offset:37888
	ds_read_b128 v[200:203], v213 offset:38912
	ds_read_b128 v[204:207], v213 offset:39936
	global_load_lds_dwordx4 v[216:217], off
	v_lshl_add_u64 v[216:217], s[6:7], 0, v[180:181]
	s_mov_b32 m0, s64
	s_nop 0
	global_load_lds_dwordx4 v[216:217], off
	s_waitcnt vmcnt(8)
	s_waitcnt lgkmcnt(0)
	s_barrier
	s_setprio 1
	s_waitcnt lgkmcnt(0)
	v_mfma_f32_16x16x32_bf16 v[140:143], v[100:103], v[162:165], v[140:143]
	v_mfma_f32_16x16x32_bf16 v[136:139], v[112:115], v[162:165], v[136:139]
	v_mfma_f32_16x16x32_bf16 v[124:127], v[100:103], v[170:173], v[124:127]
	v_mfma_f32_16x16x32_bf16 v[120:123], v[112:115], v[170:173], v[120:123]
	v_mfma_f32_16x16x32_bf16 v[92:95], v[100:103], v[192:195], v[92:95]
	v_mfma_f32_16x16x32_bf16 v[88:91], v[112:115], v[192:195], v[88:91]
	v_mfma_f32_16x16x32_bf16 v[84:87], v[100:103], v[200:203], v[84:87]
	v_mfma_f32_16x16x32_bf16 v[76:79], v[112:115], v[200:203], v[76:79]
	v_mfma_f32_16x16x32_bf16 v[140:143], v[108:111], v[166:169], v[140:143]
	v_mfma_f32_16x16x32_bf16 v[136:139], v[116:119], v[166:169], v[136:139]
	v_mfma_f32_16x16x32_bf16 v[124:127], v[108:111], v[174:177], v[124:127]
	v_mfma_f32_16x16x32_bf16 v[120:123], v[116:119], v[174:177], v[120:123]
	v_mfma_f32_16x16x32_bf16 v[92:95], v[108:111], v[196:199], v[92:95]
	v_mfma_f32_16x16x32_bf16 v[88:91], v[116:119], v[196:199], v[88:91]
	v_mfma_f32_16x16x32_bf16 v[84:87], v[108:111], v[204:207], v[84:87]
	v_mfma_f32_16x16x32_bf16 v[76:79], v[116:119], v[204:207], v[76:79]
	s_setprio 0
	s_setprio 1
	v_mfma_f32_16x16x32_bf16 v[132:135], v[146:149], v[162:165], v[132:135]
	v_mfma_f32_16x16x32_bf16 v[128:131], v[154:157], v[162:165], v[128:131]
	v_mfma_f32_16x16x32_bf16 v[104:107], v[146:149], v[170:173], v[104:107]
	v_mfma_f32_16x16x32_bf16 v[96:99], v[154:157], v[170:173], v[96:99]
	v_mfma_f32_16x16x32_bf16 v[80:83], v[146:149], v[192:195], v[80:83]
	v_mfma_f32_16x16x32_bf16 v[72:75], v[154:157], v[192:195], v[72:75]
	v_mfma_f32_16x16x32_bf16 v[68:71], v[146:149], v[200:203], v[68:71]
	v_mfma_f32_16x16x32_bf16 v[64:67], v[154:157], v[200:203], v[64:67]
	v_mfma_f32_16x16x32_bf16 v[132:135], v[150:153], v[166:169], v[132:135]
	v_mfma_f32_16x16x32_bf16 v[128:131], v[158:161], v[166:169], v[128:131]
	v_mfma_f32_16x16x32_bf16 v[104:107], v[150:153], v[174:177], v[104:107]
	v_mfma_f32_16x16x32_bf16 v[96:99], v[158:161], v[174:177], v[96:99]
	v_mfma_f32_16x16x32_bf16 v[80:83], v[150:153], v[196:199], v[80:83]
	v_mfma_f32_16x16x32_bf16 v[72:75], v[158:161], v[196:199], v[72:75]
	v_mfma_f32_16x16x32_bf16 v[68:71], v[150:153], v[204:207], v[68:71]
	v_mfma_f32_16x16x32_bf16 v[64:67], v[158:161], v[204:207], v[64:67]
	s_setprio 0
	s_barrier
	s_add_i32 s6, s73, s28
	v_lshl_add_u64 v[178:179], v[178:179], 0, s[8:9]
	s_mov_b32 m0, s6
	ds_read_b128 v[162:165], v213 offset:49152
	ds_read_b128 v[166:169], v213 offset:50176
	ds_read_b128 v[170:173], v213 offset:51200
	ds_read_b128 v[174:177], v213 offset:52224
	ds_read_b128 v[192:195], v213 offset:53248
	ds_read_b128 v[196:199], v213 offset:54272
	ds_read_b128 v[200:203], v213 offset:55296
	ds_read_b128 v[204:207], v213 offset:56320
	global_load_lds_dwordx4 v[178:179], off
	s_add_i32 m0, s6, 0x2000
	s_add_u32 s4, s4, 0x40080
	v_lshl_add_u64 v[178:179], v[208:209], 0, s[8:9]
	s_addc_u32 s5, s5, 0
	s_add_i32 s6, s74, s28
	global_load_lds_dwordx4 v[178:179], off
	v_lshl_add_u64 v[178:179], s[4:5], 0, v[182:183]
	s_mov_b32 m0, s6
	s_nop 0
	global_load_lds_dwordx4 v[178:179], off
	v_lshl_add_u64 v[178:179], s[4:5], 0, v[180:181]
	s_add_i32 m0, s6, 0x2000
	s_nop 0
	global_load_lds_dwordx4 v[178:179], off
	v_lshl_add_u64 v[178:179], v[210:211], 0, s[8:9]
	s_mov_b32 m0, s13
	s_nop 0
	global_load_lds_dwordx4 v[178:179], off
	v_lshl_add_u64 v[178:179], v[214:215], 0, s[8:9]
	s_mov_b32 m0, s65
	s_nop 0
	global_load_lds_dwordx4 v[178:179], off
	s_waitcnt vmcnt(8)
	s_waitcnt lgkmcnt(0)
	s_barrier
	s_setprio 1
	s_waitcnt lgkmcnt(0)
	v_mfma_f32_16x16x32_bf16 v[60:63], v[100:103], v[162:165], v[60:63]
	v_mfma_f32_16x16x32_bf16 v[56:59], v[112:115], v[162:165], v[56:59]
	v_mfma_f32_16x16x32_bf16 v[48:51], v[100:103], v[170:173], v[48:51]
	v_mfma_f32_16x16x32_bf16 v[44:47], v[112:115], v[170:173], v[44:47]
	v_mfma_f32_16x16x32_bf16 v[36:39], v[100:103], v[192:195], v[36:39]
	v_mfma_f32_16x16x32_bf16 v[28:31], v[112:115], v[192:195], v[28:31]
	v_mfma_f32_16x16x32_bf16 v[20:23], v[100:103], v[200:203], v[20:23]
	v_mfma_f32_16x16x32_bf16 v[12:15], v[112:115], v[200:203], v[12:15]
	v_mfma_f32_16x16x32_bf16 v[60:63], v[108:111], v[166:169], v[60:63]
	v_mfma_f32_16x16x32_bf16 v[56:59], v[116:119], v[166:169], v[56:59]
	v_mfma_f32_16x16x32_bf16 v[48:51], v[108:111], v[174:177], v[48:51]
	v_mfma_f32_16x16x32_bf16 v[44:47], v[116:119], v[174:177], v[44:47]
	v_mfma_f32_16x16x32_bf16 v[36:39], v[108:111], v[196:199], v[36:39]
	v_mfma_f32_16x16x32_bf16 v[28:31], v[116:119], v[196:199], v[28:31]
	v_mfma_f32_16x16x32_bf16 v[20:23], v[108:111], v[204:207], v[20:23]
	v_mfma_f32_16x16x32_bf16 v[12:15], v[116:119], v[204:207], v[12:15]
	s_setprio 0
	s_setprio 1
	v_mfma_f32_16x16x32_bf16 v[52:55], v[146:149], v[162:165], v[52:55]
	v_mfma_f32_16x16x32_bf16 v[40:43], v[154:157], v[162:165], v[40:43]
	v_mfma_f32_16x16x32_bf16 v[32:35], v[146:149], v[170:173], v[32:35]
	v_mfma_f32_16x16x32_bf16 v[24:27], v[154:157], v[170:173], v[24:27]
	v_mfma_f32_16x16x32_bf16 v[16:19], v[146:149], v[192:195], v[16:19]
	v_mfma_f32_16x16x32_bf16 v[8:11], v[154:157], v[192:195], v[8:11]
	v_mfma_f32_16x16x32_bf16 v[4:7], v[146:149], v[200:203], v[4:7]
	v_mfma_f32_16x16x32_bf16 v[0:3], v[154:157], v[200:203], v[0:3]
	v_mfma_f32_16x16x32_bf16 v[52:55], v[150:153], v[166:169], v[52:55]
	v_mfma_f32_16x16x32_bf16 v[40:43], v[158:161], v[166:169], v[40:43]
	v_mfma_f32_16x16x32_bf16 v[32:35], v[150:153], v[174:177], v[32:35]
	v_mfma_f32_16x16x32_bf16 v[24:27], v[158:161], v[174:177], v[24:27]
	v_mfma_f32_16x16x32_bf16 v[16:19], v[150:153], v[196:199], v[16:19]
	v_mfma_f32_16x16x32_bf16 v[8:11], v[158:161], v[196:199], v[8:11]
	v_mfma_f32_16x16x32_bf16 v[4:7], v[150:153], v[204:207], v[4:7]
	v_mfma_f32_16x16x32_bf16 v[0:3], v[158:161], v[204:207], v[0:3]
	s_setprio 0
	s_add_i32 s72, s72, 2
	s_add_u32 s70, s70, 0x100
	s_addc_u32 s71, s71, 0
	s_add_u32 s2, s2, 0x100
	s_addc_u32 s3, s3, 0
	s_add_u32 s4, s2, 0xfffc0080
	s_addc_u32 s5, s3, -1
	s_cmp_eq_u32 s72, 12
	s_cselect_b32 s7, s55, s5
	s_cselect_b32 s6, s62, s4
	s_cselect_b32 s5, s53, s71
	s_cselect_b32 s4, s63, s70
	s_cmp_gt_u32 s72, 13
	s_barrier
	s_cbranch_scc0 .LBB0_755
	s_and_b64 vcc, exec, s[50:51]
	s_cbranch_vccz .LBB0_758
	s_barrier

.LBB0_1187:
	v_mov_b32_e32 v35, v145
	v_mov_b32_e32 v39, v145
	s_add_u32 s3, s14, 0x100
	v_mov_b32_e32 v48, 0
	s_addc_u32 s14, s15, 0
	v_lshl_add_u64 v[40:41], s[54:55], 0, v[38:39]
	v_lshl_add_u64 v[42:43], s[54:55], 0, v[34:35]
	s_mov_b32 s15, -2
	s_mov_b64 s[4:5], 0
	v_mov_b32_e32 v49, v48
	v_mov_b32_e32 v50, v48
	v_mov_b32_e32 v51, v48
	v_mov_b32_e32 v56, v48
	v_mov_b32_e32 v57, v48
	v_mov_b32_e32 v58, v48
	v_mov_b32_e32 v59, v48
	v_mov_b32_e32 v64, v48
	v_mov_b32_e32 v65, v48
	v_mov_b32_e32 v66, v48
	v_mov_b32_e32 v67, v48
	v_mov_b32_e32 v72, v48
	v_mov_b32_e32 v73, v48
	v_mov_b32_e32 v74, v48
	v_mov_b32_e32 v75, v48
	v_mov_b32_e32 v0, v48
	v_mov_b32_e32 v1, v48
	v_mov_b32_e32 v2, v48
	v_mov_b32_e32 v3, v48
	v_mov_b32_e32 v8, v48
	v_mov_b32_e32 v9, v48
	v_mov_b32_e32 v10, v48
	v_mov_b32_e32 v11, v48
	v_mov_b32_e32 v16, v48
	v_mov_b32_e32 v17, v48
	v_mov_b32_e32 v18, v48
	v_mov_b32_e32 v19, v48
	v_mov_b32_e32 v24, v48
	v_mov_b32_e32 v25, v48
	v_mov_b32_e32 v26, v48
	v_mov_b32_e32 v27, v48
	v_mov_b32_e32 v52, v48
	v_mov_b32_e32 v53, v48
	v_mov_b32_e32 v54, v48
	v_mov_b32_e32 v55, v48
	v_mov_b32_e32 v60, v48
	v_mov_b32_e32 v61, v48
	v_mov_b32_e32 v62, v48
	v_mov_b32_e32 v63, v48
	v_mov_b32_e32 v68, v48
	v_mov_b32_e32 v69, v48
	v_mov_b32_e32 v70, v48
	v_mov_b32_e32 v71, v48
	v_mov_b32_e32 v76, v48
	v_mov_b32_e32 v77, v48
	v_mov_b32_e32 v78, v48
	v_mov_b32_e32 v79, v48
	v_mov_b32_e32 v80, v48
	v_mov_b32_e32 v81, v48
	v_mov_b32_e32 v82, v48
	v_mov_b32_e32 v83, v48
	v_mov_b32_e32 v88, v48
	v_mov_b32_e32 v89, v48
	v_mov_b32_e32 v90, v48
	v_mov_b32_e32 v91, v48
	v_mov_b32_e32 v96, v48
	v_mov_b32_e32 v97, v48
	v_mov_b32_e32 v98, v48
	v_mov_b32_e32 v99, v48
	v_mov_b32_e32 v104, v48
	v_mov_b32_e32 v105, v48
	v_mov_b32_e32 v106, v48
	v_mov_b32_e32 v107, v48
	v_mov_b32_e32 v112, v48
	v_mov_b32_e32 v113, v48
	v_mov_b32_e32 v114, v48
	v_mov_b32_e32 v115, v48
	v_mov_b32_e32 v120, v48
	v_mov_b32_e32 v121, v48
	v_mov_b32_e32 v122, v48
	v_mov_b32_e32 v123, v48
	v_mov_b32_e32 v128, v48
	v_mov_b32_e32 v129, v48
	v_mov_b32_e32 v130, v48
	v_mov_b32_e32 v131, v48
	v_mov_b32_e32 v136, v48
	v_mov_b32_e32 v137, v48
	v_mov_b32_e32 v138, v48
	v_mov_b32_e32 v139, v48
	v_mov_b32_e32 v84, v48
	v_mov_b32_e32 v85, v48
	v_mov_b32_e32 v86, v48
	v_mov_b32_e32 v87, v48
	v_mov_b32_e32 v92, v48
	v_mov_b32_e32 v93, v48
	v_mov_b32_e32 v94, v48
	v_mov_b32_e32 v95, v48
	v_mov_b32_e32 v100, v48
	v_mov_b32_e32 v101, v48
	v_mov_b32_e32 v102, v48
	v_mov_b32_e32 v103, v48
	v_mov_b32_e32 v108, v48
	v_mov_b32_e32 v109, v48
	v_mov_b32_e32 v110, v48
	v_mov_b32_e32 v111, v48
	v_mov_b32_e32 v116, v48
	v_mov_b32_e32 v117, v48
	v_mov_b32_e32 v118, v48
	v_mov_b32_e32 v119, v48
	v_mov_b32_e32 v124, v48
	v_mov_b32_e32 v125, v48
	v_mov_b32_e32 v126, v48
	v_mov_b32_e32 v127, v48
	v_mov_b32_e32 v132, v48
	v_mov_b32_e32 v133, v48
	v_mov_b32_e32 v134, v48
	v_mov_b32_e32 v135, v48
	v_mov_b32_e32 v140, v48
	v_mov_b32_e32 v141, v48
	v_mov_b32_e32 v142, v48
	v_mov_b32_e32 v143, v48
	v_mov_b32_e32 v28, v48
	v_mov_b32_e32 v29, v48
	v_mov_b32_e32 v30, v48
	v_mov_b32_e32 v31, v48
	v_mov_b32_e32 v20, v48
	v_mov_b32_e32 v21, v48
	v_mov_b32_e32 v22, v48
	v_mov_b32_e32 v23, v48
	v_mov_b32_e32 v12, v48
	v_mov_b32_e32 v13, v48
	v_mov_b32_e32 v14, v48
	v_mov_b32_e32 v15, v48
	v_mov_b32_e32 v4, v48
	v_mov_b32_e32 v5, v48
	v_mov_b32_e32 v6, v48
	v_mov_b32_e32 v7, v48
	s_add_u32 s6, s40, s4
	s_addc_u32 s7, s41, s5
	s_add_u32 s10, s6, 0x2cc98900
	s_addc_u32 s11, s7, 0
	s_add_u32 s88, s3, s4
	s_addc_u32 s89, s14, s5
	s_cmpk_eq_i32 s4, 0x300
	s_cselect_b64 vcc, -1, 0
	s_and_b64 s[6:7], vcc, exec
	s_cselect_b32 s11, s45, s11
	s_cselect_b32 s10, s44, s10
	s_cselect_b32 s7, s61, s89
	s_cselect_b32 s6, s60, s88
.LBB0_1188:
	s_add_i32 s59, 0, 0x10000
	v_add_u32_e32 v37, s59, v161
	s_add_i32 s63, 0, 0x14000
	ds_read_b128 v[44:47], v37
	ds_read_b128 v[170:173], v37 offset:1024
	ds_read_b128 v[174:177], v37 offset:2048
	ds_read_b128 v[178:181], v37 offset:3072
	v_add_u32_e32 v37, s63, v161
	ds_read_b128 v[182:185], v37
	ds_read_b128 v[186:189], v37 offset:1024
	ds_read_b128 v[190:193], v37 offset:2048
	ds_read_b128 v[194:197], v37 offset:3072
	v_cndmask_b32_e32 v144, v32, v166, vcc
	v_cndmask_b32_e32 v33, v34, v167, vcc
	v_cndmask_b32_e32 v154, v36, v168, vcc
	v_cndmask_b32_e32 v35, v38, v169, vcc
	v_lshl_add_u64 v[230:231], v[42:43], 0, s[4:5]
	s_add_i32 m0, s17, 0xc000
	ds_read_b128 v[198:201], v165
	ds_read_b128 v[202:205], v165 offset:1024
	ds_read_b128 v[206:209], v165 offset:2048
	ds_read_b128 v[210:213], v165 offset:3072
	ds_read_b128 v[214:217], v165 offset:4096
	ds_read_b128 v[218:221], v165 offset:5120
	ds_read_b128 v[222:225], v165 offset:6144
	ds_read_b128 v[226:229], v165 offset:7168
	global_load_lds_dwordx4 v[230:231], off
	v_lshl_add_u64 v[230:231], v[40:41], 0, s[4:5]
	s_add_i32 m0, s17, 0xe000
	s_nop 0
	global_load_lds_dwordx4 v[230:231], off
	s_waitcnt vmcnt(8)
	s_waitcnt lgkmcnt(0)
	s_barrier
	s_setprio 1
	s_waitcnt lgkmcnt(0)
	v_mfma_i32_16x16x64_i8 v[140:143], v[44:47], v[198:201], v[140:143]
	v_mfma_i32_16x16x64_i8 v[132:135], v[174:177], v[198:201], v[132:135]
	v_mfma_i32_16x16x64_i8 v[124:127], v[44:47], v[206:209], v[124:127]
	v_mfma_i32_16x16x64_i8 v[116:119], v[174:177], v[206:209], v[116:119]
	v_mfma_i32_16x16x64_i8 v[108:111], v[44:47], v[214:217], v[108:111]
	v_mfma_i32_16x16x64_i8 v[100:103], v[174:177], v[214:217], v[100:103]
	v_mfma_i32_16x16x64_i8 v[92:95], v[44:47], v[222:225], v[92:95]
	v_mfma_i32_16x16x64_i8 v[84:87], v[174:177], v[222:225], v[84:87]
	v_mfma_i32_16x16x64_i8 v[140:143], v[170:173], v[202:205], v[140:143]
	v_mfma_i32_16x16x64_i8 v[132:135], v[178:181], v[202:205], v[132:135]
	v_mfma_i32_16x16x64_i8 v[124:127], v[170:173], v[210:213], v[124:127]
	v_mfma_i32_16x16x64_i8 v[116:119], v[178:181], v[210:213], v[116:119]
	v_mfma_i32_16x16x64_i8 v[108:111], v[170:173], v[218:221], v[108:111]
	v_mfma_i32_16x16x64_i8 v[100:103], v[178:181], v[218:221], v[100:103]
	v_mfma_i32_16x16x64_i8 v[92:95], v[170:173], v[226:229], v[92:95]
	v_mfma_i32_16x16x64_i8 v[84:87], v[178:181], v[226:229], v[84:87]
	s_setprio 0
	s_setprio 1
	v_mfma_i32_16x16x64_i8 v[136:139], v[182:185], v[198:201], v[136:139]
	v_mfma_i32_16x16x64_i8 v[128:131], v[190:193], v[198:201], v[128:131]
	v_mfma_i32_16x16x64_i8 v[120:123], v[182:185], v[206:209], v[120:123]
	v_mfma_i32_16x16x64_i8 v[112:115], v[190:193], v[206:209], v[112:115]
	v_mfma_i32_16x16x64_i8 v[104:107], v[182:185], v[214:217], v[104:107]
	v_mfma_i32_16x16x64_i8 v[96:99], v[190:193], v[214:217], v[96:99]
	v_mfma_i32_16x16x64_i8 v[88:91], v[182:185], v[222:225], v[88:91]
	v_mfma_i32_16x16x64_i8 v[80:83], v[190:193], v[222:225], v[80:83]
	v_mfma_i32_16x16x64_i8 v[136:139], v[186:189], v[202:205], v[136:139]
	v_mfma_i32_16x16x64_i8 v[128:131], v[194:197], v[202:205], v[128:131]
	v_mfma_i32_16x16x64_i8 v[120:123], v[186:189], v[210:213], v[120:123]
	v_mfma_i32_16x16x64_i8 v[112:115], v[194:197], v[210:213], v[112:115]
	v_mfma_i32_16x16x64_i8 v[104:107], v[186:189], v[218:221], v[104:107]
	v_mfma_i32_16x16x64_i8 v[96:99], v[194:197], v[218:221], v[96:99]
	v_mfma_i32_16x16x64_i8 v[88:91], v[186:189], v[226:229], v[88:91]
	v_mfma_i32_16x16x64_i8 v[80:83], v[194:197], v[226:229], v[80:83]
	s_setprio 0
	s_barrier
	s_add_i32 s59, s59, s16
	v_lshl_add_u64 v[230:231], s[6:7], 0, v[146:147]
	s_mov_b32 m0, s59
	ds_read_b128 v[198:201], v165 offset:16384
	ds_read_b128 v[202:205], v165 offset:17408
	ds_read_b128 v[206:209], v165 offset:18432
	ds_read_b128 v[210:213], v165 offset:19456
	ds_read_b128 v[214:217], v165 offset:20480
	ds_read_b128 v[218:221], v165 offset:21504
	ds_read_b128 v[222:225], v165 offset:22528
	ds_read_b128 v[226:229], v165 offset:23552
	global_load_lds_dwordx4 v[230:231], off
	s_add_i32 m0, s59, 0x2000
	s_add_u32 s68, s6, 0x20000
	v_lshl_add_u64 v[232:233], s[6:7], 0, v[148:149]
	s_addc_u32 s69, s7, 0
	s_add_i32 s59, s63, s16
	global_load_lds_dwordx4 v[232:233], off
	v_lshl_add_u64 v[234:235], s[68:69], 0, v[146:147]
	s_mov_b32 m0, s59
	v_mov_b32_e32 v155, v145
	global_load_lds_dwordx4 v[234:235], off
	v_lshl_add_u64 v[234:235], s[68:69], 0, v[148:149]
	s_add_i32 m0, s59, 0x2000
	s_nop 0
	global_load_lds_dwordx4 v[234:235], off
	s_mov_b32 m0, s17
	v_lshl_add_u64 v[234:235], s[10:11], 0, v[144:145]
	global_load_lds_dwordx4 v144, s[10:11]
	s_mov_b32 m0, s20
	s_nop 0
	global_load_lds_dwordx4 v154, s[10:11]
	s_waitcnt vmcnt(8)
	s_waitcnt lgkmcnt(0)
	v_lshl_add_u64 v[154:155], s[10:11], 0, v[154:155]
	s_barrier
	s_setprio 1
	s_waitcnt lgkmcnt(0)
	v_mfma_i32_16x16x64_i8 v[76:79], v[44:47], v[198:201], v[76:79]
	v_mfma_i32_16x16x64_i8 v[68:71], v[174:177], v[198:201], v[68:71]
	v_mfma_i32_16x16x64_i8 v[60:63], v[44:47], v[206:209], v[60:63]
	v_mfma_i32_16x16x64_i8 v[52:55], v[174:177], v[206:209], v[52:55]
	v_mfma_i32_16x16x64_i8 v[24:27], v[44:47], v[214:217], v[24:27]
	v_mfma_i32_16x16x64_i8 v[16:19], v[174:177], v[214:217], v[16:19]
	v_mfma_i32_16x16x64_i8 v[8:11], v[44:47], v[222:225], v[8:11]
	v_mfma_i32_16x16x64_i8 v[0:3], v[174:177], v[222:225], v[0:3]
	v_mfma_i32_16x16x64_i8 v[76:79], v[170:173], v[202:205], v[76:79]
	v_mfma_i32_16x16x64_i8 v[68:71], v[178:181], v[202:205], v[68:71]
	v_mfma_i32_16x16x64_i8 v[60:63], v[170:173], v[210:213], v[60:63]
	v_mfma_i32_16x16x64_i8 v[52:55], v[178:181], v[210:213], v[52:55]
	v_mfma_i32_16x16x64_i8 v[24:27], v[170:173], v[218:221], v[24:27]
	v_mfma_i32_16x16x64_i8 v[16:19], v[178:181], v[218:221], v[16:19]
	v_mfma_i32_16x16x64_i8 v[8:11], v[170:173], v[226:229], v[8:11]
	v_mfma_i32_16x16x64_i8 v[0:3], v[178:181], v[226:229], v[0:3]
	s_setprio 0
	s_setprio 1
	v_mfma_i32_16x16x64_i8 v[64:67], v[190:193], v[198:201], v[64:67]
	v_mfma_i32_16x16x64_i8 v[56:59], v[182:185], v[206:209], v[56:59]
	v_mfma_i32_16x16x64_i8 v[48:51], v[190:193], v[206:209], v[48:51]
	v_mfma_i32_16x16x64_i8 v[28:31], v[182:185], v[214:217], v[28:31]
	v_mfma_i32_16x16x64_i8 v[20:23], v[190:193], v[214:217], v[20:23]
	v_mfma_i32_16x16x64_i8 v[12:15], v[182:185], v[222:225], v[12:15]
	v_mfma_i32_16x16x64_i8 v[4:7], v[190:193], v[222:225], v[4:7]
	v_mfma_i32_16x16x64_i8 v[44:47], v[182:185], v[198:201], v[72:75]
	v_mfma_i32_16x16x64_i8 v[64:67], v[194:197], v[202:205], v[64:67]
	v_mfma_i32_16x16x64_i8 v[56:59], v[186:189], v[210:213], v[56:59]
	v_mfma_i32_16x16x64_i8 v[48:51], v[194:197], v[210:213], v[48:51]
	v_mfma_i32_16x16x64_i8 v[28:31], v[186:189], v[218:221], v[28:31]
	v_mfma_i32_16x16x64_i8 v[20:23], v[194:197], v[218:221], v[20:23]
	v_mfma_i32_16x16x64_i8 v[12:15], v[186:189], v[226:229], v[12:15]
	v_mfma_i32_16x16x64_i8 v[4:7], v[194:197], v[226:229], v[4:7]
	v_mfma_i32_16x16x64_i8 v[44:47], v[186:189], v[202:205], v[44:47]
	s_setprio 0
	s_barrier
	s_add_i32 s59, 0, 0x18000
	v_add_u32_e32 v37, s59, v161
	s_add_i32 s63, 0, 0x1c000
	ds_read_b128 v[72:75], v37
	ds_read_b128 v[170:173], v37 offset:1024
	ds_read_b128 v[174:177], v37 offset:2048
	ds_read_b128 v[178:181], v37 offset:3072
	v_add_u32_e32 v37, s63, v161
	ds_read_b128 v[182:185], v37
	ds_read_b128 v[186:189], v37 offset:1024
	ds_read_b128 v[190:193], v37 offset:2048
	ds_read_b128 v[194:197], v37 offset:3072
	s_mov_b32 m0, s21
	ds_read_b128 v[198:201], v165 offset:32768
	ds_read_b128 v[202:205], v165 offset:33792
	ds_read_b128 v[206:209], v165 offset:34816
	ds_read_b128 v[210:213], v165 offset:35840
	ds_read_b128 v[214:217], v165 offset:36864
	ds_read_b128 v[218:221], v165 offset:37888
	ds_read_b128 v[222:225], v165 offset:38912
	ds_read_b128 v[226:229], v165 offset:39936
	global_load_lds_dwordx4 v33, s[10:11]
	s_mov_b32 m0, s34
	s_nop 0
	global_load_lds_dwordx4 v35, s[10:11]
	s_waitcnt vmcnt(8)
	s_waitcnt lgkmcnt(0)
	s_barrier
	s_setprio 1
	s_waitcnt lgkmcnt(0)
	v_mfma_i32_16x16x64_i8 v[140:143], v[72:75], v[198:201], v[140:143]
	v_mfma_i32_16x16x64_i8 v[132:135], v[174:177], v[198:201], v[132:135]
	v_mfma_i32_16x16x64_i8 v[124:127], v[72:75], v[206:209], v[124:127]
	v_mfma_i32_16x16x64_i8 v[116:119], v[174:177], v[206:209], v[116:119]
	v_mfma_i32_16x16x64_i8 v[108:111], v[72:75], v[214:217], v[108:111]
	v_mfma_i32_16x16x64_i8 v[100:103], v[174:177], v[214:217], v[100:103]
	v_mfma_i32_16x16x64_i8 v[92:95], v[72:75], v[222:225], v[92:95]
	v_mfma_i32_16x16x64_i8 v[84:87], v[174:177], v[222:225], v[84:87]
	v_mfma_i32_16x16x64_i8 v[140:143], v[170:173], v[202:205], v[140:143]
	v_mfma_i32_16x16x64_i8 v[132:135], v[178:181], v[202:205], v[132:135]
	v_mfma_i32_16x16x64_i8 v[124:127], v[170:173], v[210:213], v[124:127]
	v_mfma_i32_16x16x64_i8 v[116:119], v[178:181], v[210:213], v[116:119]
	v_mfma_i32_16x16x64_i8 v[108:111], v[170:173], v[218:221], v[108:111]
	v_mfma_i32_16x16x64_i8 v[100:103], v[178:181], v[218:221], v[100:103]
	v_mfma_i32_16x16x64_i8 v[92:95], v[170:173], v[226:229], v[92:95]
	v_mfma_i32_16x16x64_i8 v[84:87], v[178:181], v[226:229], v[84:87]
	s_setprio 0
	s_setprio 1
	v_mfma_i32_16x16x64_i8 v[136:139], v[182:185], v[198:201], v[136:139]
	v_mfma_i32_16x16x64_i8 v[128:131], v[190:193], v[198:201], v[128:131]
	v_mfma_i32_16x16x64_i8 v[120:123], v[182:185], v[206:209], v[120:123]
	v_mfma_i32_16x16x64_i8 v[112:115], v[190:193], v[206:209], v[112:115]
	v_mfma_i32_16x16x64_i8 v[104:107], v[182:185], v[214:217], v[104:107]
	v_mfma_i32_16x16x64_i8 v[96:99], v[190:193], v[214:217], v[96:99]
	v_mfma_i32_16x16x64_i8 v[88:91], v[182:185], v[222:225], v[88:91]
	v_mfma_i32_16x16x64_i8 v[80:83], v[190:193], v[222:225], v[80:83]
	v_mfma_i32_16x16x64_i8 v[136:139], v[186:189], v[202:205], v[136:139]
	v_mfma_i32_16x16x64_i8 v[128:131], v[194:197], v[202:205], v[128:131]
	v_mfma_i32_16x16x64_i8 v[120:123], v[186:189], v[210:213], v[120:123]
	v_mfma_i32_16x16x64_i8 v[112:115], v[194:197], v[210:213], v[112:115]
	v_mfma_i32_16x16x64_i8 v[104:107], v[186:189], v[218:221], v[104:107]
	v_mfma_i32_16x16x64_i8 v[96:99], v[194:197], v[218:221], v[96:99]
	v_mfma_i32_16x16x64_i8 v[88:91], v[186:189], v[226:229], v[88:91]
	v_mfma_i32_16x16x64_i8 v[80:83], v[194:197], v[226:229], v[80:83]
	s_setprio 0
	s_barrier
	s_add_i32 s10, s59, s16
	v_lshl_add_u64 v[230:231], v[230:231], 0, s[8:9]
	s_mov_b32 m0, s10
	ds_read_b128 v[198:201], v165 offset:49152
	ds_read_b128 v[202:205], v165 offset:50176
	ds_read_b128 v[206:209], v165 offset:51200
	ds_read_b128 v[210:213], v165 offset:52224
	ds_read_b128 v[214:217], v165 offset:53248
	ds_read_b128 v[218:221], v165 offset:54272
	ds_read_b128 v[222:225], v165 offset:55296
	ds_read_b128 v[226:229], v165 offset:56320
	global_load_lds_dwordx4 v[230:231], off
	s_add_i32 m0, s10, 0x2000
	s_add_u32 s6, s6, 0x20080
	v_lshl_add_u64 v[230:231], v[232:233], 0, s[8:9]
	s_addc_u32 s7, s7, 0
	s_add_i32 s10, s63, s16
	global_load_lds_dwordx4 v[230:231], off
	v_lshl_add_u64 v[230:231], s[6:7], 0, v[146:147]
	s_mov_b32 m0, s10
	v_lshl_add_u64 v[154:155], v[154:155], 0, s[8:9]
	global_load_lds_dwordx4 v[230:231], off
	v_lshl_add_u64 v[230:231], s[6:7], 0, v[148:149]
	s_add_i32 m0, s10, 0x2000
	s_nop 0
	global_load_lds_dwordx4 v[230:231], off
	v_lshl_add_u64 v[230:231], v[234:235], 0, s[8:9]
	s_mov_b32 m0, s12
	s_nop 0
	global_load_lds_dwordx4 v[230:231], off
	s_mov_b32 m0, s13
	s_nop 0
	global_load_lds_dwordx4 v[154:155], off
	s_waitcnt vmcnt(8)
	s_waitcnt lgkmcnt(0)
	s_barrier
	s_setprio 1
	s_waitcnt lgkmcnt(0)
	v_mfma_i32_16x16x64_i8 v[76:79], v[72:75], v[198:201], v[76:79]
	v_mfma_i32_16x16x64_i8 v[68:71], v[174:177], v[198:201], v[68:71]
	v_mfma_i32_16x16x64_i8 v[60:63], v[72:75], v[206:209], v[60:63]
	v_mfma_i32_16x16x64_i8 v[52:55], v[174:177], v[206:209], v[52:55]
	v_mfma_i32_16x16x64_i8 v[24:27], v[72:75], v[214:217], v[24:27]
	v_mfma_i32_16x16x64_i8 v[16:19], v[174:177], v[214:217], v[16:19]
	v_mfma_i32_16x16x64_i8 v[8:11], v[72:75], v[222:225], v[8:11]
	v_mfma_i32_16x16x64_i8 v[0:3], v[174:177], v[222:225], v[0:3]
	v_mfma_i32_16x16x64_i8 v[76:79], v[170:173], v[202:205], v[76:79]
	v_mfma_i32_16x16x64_i8 v[68:71], v[178:181], v[202:205], v[68:71]
	v_mfma_i32_16x16x64_i8 v[60:63], v[170:173], v[210:213], v[60:63]
	v_mfma_i32_16x16x64_i8 v[52:55], v[178:181], v[210:213], v[52:55]
	v_mfma_i32_16x16x64_i8 v[24:27], v[170:173], v[218:221], v[24:27]
	v_mfma_i32_16x16x64_i8 v[16:19], v[178:181], v[218:221], v[16:19]
	v_mfma_i32_16x16x64_i8 v[8:11], v[170:173], v[226:229], v[8:11]
	v_mfma_i32_16x16x64_i8 v[0:3], v[178:181], v[226:229], v[0:3]
	s_setprio 0
	s_setprio 1
	v_mfma_i32_16x16x64_i8 v[44:47], v[182:185], v[198:201], v[44:47]
	v_mfma_i32_16x16x64_i8 v[72:75], v[186:189], v[202:205], v[44:47]
	v_mfma_i32_16x16x64_i8 v[44:47], v[190:193], v[198:201], v[64:67]
	v_mfma_i32_16x16x64_i8 v[64:67], v[194:197], v[202:205], v[44:47]
	v_mfma_i32_16x16x64_i8 v[44:47], v[182:185], v[206:209], v[56:59]
	v_mfma_i32_16x16x64_i8 v[56:59], v[186:189], v[210:213], v[44:47]
	v_mfma_i32_16x16x64_i8 v[44:47], v[190:193], v[206:209], v[48:51]
	v_mfma_i32_16x16x64_i8 v[28:31], v[182:185], v[214:217], v[28:31]
	v_mfma_i32_16x16x64_i8 v[20:23], v[190:193], v[214:217], v[20:23]
	v_mfma_i32_16x16x64_i8 v[12:15], v[182:185], v[222:225], v[12:15]
	v_mfma_i32_16x16x64_i8 v[4:7], v[190:193], v[222:225], v[4:7]
	v_mfma_i32_16x16x64_i8 v[48:51], v[194:197], v[210:213], v[44:47]
	v_mfma_i32_16x16x64_i8 v[28:31], v[186:189], v[218:221], v[28:31]
	v_mfma_i32_16x16x64_i8 v[20:23], v[194:197], v[218:221], v[20:23]
	v_mfma_i32_16x16x64_i8 v[12:15], v[186:189], v[226:229], v[12:15]
	v_mfma_i32_16x16x64_i8 v[4:7], v[194:197], v[226:229], v[4:7]
	s_setprio 0
	s_add_i32 s15, s15, 2
	s_add_u32 s4, s4, 0x100
	s_addc_u32 s5, s5, 0
	s_add_u32 s6, s40, s4
	s_addc_u32 s7, s41, s5
	s_add_u32 s10, s6, 0x2cc98900
	s_addc_u32 s11, s7, 0
	s_add_u32 s88, s3, s4
	s_addc_u32 s89, s14, s5
	s_cmpk_eq_i32 s4, 0x300
	s_cselect_b64 vcc, -1, 0
	s_and_b64 s[6:7], vcc, exec
	s_cselect_b32 s11, s45, s11
	s_cselect_b32 s10, s44, s10
	s_cselect_b32 s7, s61, s89
	s_cselect_b32 s6, s60, s88
	s_cmp_gt_u32 s15, 5
	s_barrier
	s_cbranch_scc0 .LBB0_1188
	s_and_b64 vcc, exec, s[56:57]
	s_cbranch_vccz .LBB0_1191
	s_barrier

.LBB0_1297:
	s_add_u32 s61, s4, 0x100
	v_mov_b32_e32 v0, 0
	s_addc_u32 s62, s5, 0
	s_mov_b32 s63, -2
	v_mov_b32_e32 v1, v0
	v_mov_b32_e32 v2, v0
	v_mov_b32_e32 v3, v0
	v_mov_b32_e32 v4, v0
	v_mov_b32_e32 v5, v0
	v_mov_b32_e32 v6, v0
	v_mov_b32_e32 v7, v0
	v_mov_b32_e32 v16, v0
	v_mov_b32_e32 v17, v0
	v_mov_b32_e32 v18, v0
	v_mov_b32_e32 v19, v0
	v_mov_b32_e32 v20, v0
	v_mov_b32_e32 v21, v0
	v_mov_b32_e32 v22, v0
	v_mov_b32_e32 v23, v0
	v_mov_b32_e32 v32, v0
	v_mov_b32_e32 v33, v0
	v_mov_b32_e32 v34, v0
	v_mov_b32_e32 v35, v0
	v_mov_b32_e32 v36, v0
	v_mov_b32_e32 v37, v0
	v_mov_b32_e32 v38, v0
	v_mov_b32_e32 v39, v0
	v_mov_b32_e32 v48, v0
	v_mov_b32_e32 v49, v0
	v_mov_b32_e32 v50, v0
	v_mov_b32_e32 v51, v0
	v_mov_b32_e32 v52, v0
	v_mov_b32_e32 v53, v0
	v_mov_b32_e32 v54, v0
	v_mov_b32_e32 v55, v0
	v_mov_b32_e32 v8, v0
	v_mov_b32_e32 v9, v0
	v_mov_b32_e32 v10, v0
	v_mov_b32_e32 v11, v0
	v_mov_b32_e32 v12, v0
	v_mov_b32_e32 v13, v0
	v_mov_b32_e32 v14, v0
	v_mov_b32_e32 v15, v0
	v_mov_b32_e32 v24, v0
	v_mov_b32_e32 v25, v0
	v_mov_b32_e32 v26, v0
	v_mov_b32_e32 v27, v0
	v_mov_b32_e32 v28, v0
	v_mov_b32_e32 v29, v0
	v_mov_b32_e32 v30, v0
	v_mov_b32_e32 v31, v0
	v_mov_b32_e32 v40, v0
	v_mov_b32_e32 v41, v0
	v_mov_b32_e32 v42, v0
	v_mov_b32_e32 v43, v0
	v_mov_b32_e32 v44, v0
	v_mov_b32_e32 v45, v0
	v_mov_b32_e32 v46, v0
	v_mov_b32_e32 v47, v0
	v_mov_b32_e32 v56, v0
	v_mov_b32_e32 v57, v0
	v_mov_b32_e32 v58, v0
	v_mov_b32_e32 v59, v0
	v_mov_b32_e32 v60, v0
	v_mov_b32_e32 v61, v0
	v_mov_b32_e32 v62, v0
	v_mov_b32_e32 v63, v0
	v_mov_b32_e32 v64, v0
	v_mov_b32_e32 v65, v0
	v_mov_b32_e32 v66, v0
	v_mov_b32_e32 v67, v0
	v_mov_b32_e32 v68, v0
	v_mov_b32_e32 v69, v0
	v_mov_b32_e32 v70, v0
	v_mov_b32_e32 v71, v0
	v_mov_b32_e32 v80, v0
	v_mov_b32_e32 v81, v0
	v_mov_b32_e32 v82, v0
	v_mov_b32_e32 v83, v0
	v_mov_b32_e32 v84, v0
	v_mov_b32_e32 v85, v0
	v_mov_b32_e32 v86, v0
	v_mov_b32_e32 v87, v0
	v_mov_b32_e32 v96, v0
	v_mov_b32_e32 v97, v0
	v_mov_b32_e32 v98, v0
	v_mov_b32_e32 v99, v0
	v_mov_b32_e32 v100, v0
	v_mov_b32_e32 v101, v0
	v_mov_b32_e32 v102, v0
	v_mov_b32_e32 v103, v0
	v_mov_b32_e32 v112, v0
	v_mov_b32_e32 v113, v0
	v_mov_b32_e32 v114, v0
	v_mov_b32_e32 v115, v0
	v_mov_b32_e32 v116, v0
	v_mov_b32_e32 v117, v0
	v_mov_b32_e32 v118, v0
	v_mov_b32_e32 v119, v0
	v_mov_b32_e32 v72, v0
	v_mov_b32_e32 v73, v0
	v_mov_b32_e32 v74, v0
	v_mov_b32_e32 v75, v0
	v_mov_b32_e32 v76, v0
	v_mov_b32_e32 v77, v0
	v_mov_b32_e32 v78, v0
	v_mov_b32_e32 v79, v0
	v_mov_b32_e32 v88, v0
	v_mov_b32_e32 v89, v0
	v_mov_b32_e32 v90, v0
	v_mov_b32_e32 v91, v0
	v_mov_b32_e32 v92, v0
	v_mov_b32_e32 v93, v0
	v_mov_b32_e32 v94, v0
	v_mov_b32_e32 v95, v0
	v_mov_b32_e32 v104, v0
	v_mov_b32_e32 v105, v0
	v_mov_b32_e32 v106, v0
	v_mov_b32_e32 v107, v0
	v_mov_b32_e32 v108, v0
	v_mov_b32_e32 v109, v0
	v_mov_b32_e32 v110, v0
	v_mov_b32_e32 v111, v0
	v_mov_b32_e32 v120, v0
	v_mov_b32_e32 v121, v0
	v_mov_b32_e32 v122, v0
	v_mov_b32_e32 v123, v0
	v_mov_b32_e32 v124, v0
	v_mov_b32_e32 v125, v0
	v_mov_b32_e32 v126, v0
	v_mov_b32_e32 v127, v0
	s_add_u32 s4, s2, 0x100
	s_addc_u32 s5, s3, 0
	s_cmp_eq_u32 s63, 18
	s_cselect_b32 s11, s53, s5
	s_cselect_b32 s10, s52, s4
	s_cselect_b32 s7, s55, s62
	s_cselect_b32 s6, s54, s61
.LBB0_1298:
	s_add_i32 s64, 0, 0x10000
	v_add_u32_e32 v136, s64, v139
	s_add_i32 s65, 0, 0x14000
	ds_read_b128 v[146:149], v136
	ds_read_b128 v[150:153], v136 offset:1024
	ds_read_b128 v[154:157], v136 offset:2048
	ds_read_b128 v[158:161], v136 offset:3072
	v_add_u32_e32 v136, s65, v139
	ds_read_b128 v[162:165], v136
	ds_read_b128 v[166:169], v136 offset:1024
	ds_read_b128 v[170:173], v136 offset:2048
	ds_read_b128 v[174:177], v136 offset:3072
	v_lshl_add_u64 v[136:137], s[2:3], 0, v[134:135]
	s_add_i32 m0, s21, 0xc000
	ds_read_b128 v[178:181], v143
	ds_read_b128 v[182:185], v143 offset:1024
	ds_read_b128 v[186:189], v143 offset:2048
	ds_read_b128 v[190:193], v143 offset:3072
	ds_read_b128 v[194:197], v143 offset:4096
	ds_read_b128 v[198:201], v143 offset:5120
	ds_read_b128 v[202:205], v143 offset:6144
	ds_read_b128 v[206:209], v143 offset:7168
	global_load_lds_dwordx4 v[136:137], off
	v_lshl_add_u64 v[136:137], s[2:3], 0, v[132:133]
	s_add_i32 m0, s21, 0xe000
	s_nop 0
	global_load_lds_dwordx4 v[136:137], off
	s_waitcnt vmcnt(8)
	s_waitcnt lgkmcnt(0)
	s_barrier
	s_setprio 1
	s_waitcnt lgkmcnt(0)
	v_mfma_f32_16x16x32_bf16 v[124:127], v[146:149], v[178:181], v[124:127]
	v_mfma_f32_16x16x32_bf16 v[120:123], v[154:157], v[178:181], v[120:123]
	v_mfma_f32_16x16x32_bf16 v[108:111], v[146:149], v[186:189], v[108:111]
	v_mfma_f32_16x16x32_bf16 v[104:107], v[154:157], v[186:189], v[104:107]
	v_mfma_f32_16x16x32_bf16 v[92:95], v[146:149], v[194:197], v[92:95]
	v_mfma_f32_16x16x32_bf16 v[88:91], v[154:157], v[194:197], v[88:91]
	v_mfma_f32_16x16x32_bf16 v[76:79], v[146:149], v[202:205], v[76:79]
	v_mfma_f32_16x16x32_bf16 v[72:75], v[154:157], v[202:205], v[72:75]
	v_mfma_f32_16x16x32_bf16 v[124:127], v[150:153], v[182:185], v[124:127]
	v_mfma_f32_16x16x32_bf16 v[120:123], v[158:161], v[182:185], v[120:123]
	v_mfma_f32_16x16x32_bf16 v[108:111], v[150:153], v[190:193], v[108:111]
	v_mfma_f32_16x16x32_bf16 v[104:107], v[158:161], v[190:193], v[104:107]
	v_mfma_f32_16x16x32_bf16 v[92:95], v[150:153], v[198:201], v[92:95]
	v_mfma_f32_16x16x32_bf16 v[88:91], v[158:161], v[198:201], v[88:91]
	v_mfma_f32_16x16x32_bf16 v[76:79], v[150:153], v[206:209], v[76:79]
	v_mfma_f32_16x16x32_bf16 v[72:75], v[158:161], v[206:209], v[72:75]
	s_setprio 0
	s_setprio 1
	v_mfma_f32_16x16x32_bf16 v[116:119], v[162:165], v[178:181], v[116:119]
	v_mfma_f32_16x16x32_bf16 v[112:115], v[170:173], v[178:181], v[112:115]
	v_mfma_f32_16x16x32_bf16 v[100:103], v[162:165], v[186:189], v[100:103]
	v_mfma_f32_16x16x32_bf16 v[96:99], v[170:173], v[186:189], v[96:99]
	v_mfma_f32_16x16x32_bf16 v[84:87], v[162:165], v[194:197], v[84:87]
	v_mfma_f32_16x16x32_bf16 v[80:83], v[170:173], v[194:197], v[80:83]
	v_mfma_f32_16x16x32_bf16 v[68:71], v[162:165], v[202:205], v[68:71]
	v_mfma_f32_16x16x32_bf16 v[64:67], v[170:173], v[202:205], v[64:67]
	v_mfma_f32_16x16x32_bf16 v[116:119], v[166:169], v[182:185], v[116:119]
	v_mfma_f32_16x16x32_bf16 v[112:115], v[174:177], v[182:185], v[112:115]
	v_mfma_f32_16x16x32_bf16 v[100:103], v[166:169], v[190:193], v[100:103]
	v_mfma_f32_16x16x32_bf16 v[96:99], v[174:177], v[190:193], v[96:99]
	v_mfma_f32_16x16x32_bf16 v[84:87], v[166:169], v[198:201], v[84:87]
	v_mfma_f32_16x16x32_bf16 v[80:83], v[174:177], v[198:201], v[80:83]
	v_mfma_f32_16x16x32_bf16 v[68:71], v[166:169], v[206:209], v[68:71]
	v_mfma_f32_16x16x32_bf16 v[64:67], v[174:177], v[206:209], v[64:67]
	s_setprio 0
	s_barrier
	s_add_i32 s2, s64, s20
	v_lshl_add_u64 v[136:137], s[6:7], 0, v[128:129]
	s_mov_b32 m0, s2
	ds_read_b128 v[178:181], v143 offset:16384
	ds_read_b128 v[182:185], v143 offset:17408
	ds_read_b128 v[186:189], v143 offset:18432
	ds_read_b128 v[190:193], v143 offset:19456
	ds_read_b128 v[194:197], v143 offset:20480
	ds_read_b128 v[198:201], v143 offset:21504
	ds_read_b128 v[202:205], v143 offset:22528
	ds_read_b128 v[206:209], v143 offset:23552
	global_load_lds_dwordx4 v[136:137], off
	s_add_i32 m0, s2, 0x2000
	s_add_u32 s2, s6, 0x58000
	v_lshl_add_u64 v[210:211], s[6:7], 0, v[130:131]
	s_addc_u32 s3, s7, 0
	s_add_i32 s64, s65, s20
	global_load_lds_dwordx4 v[210:211], off
	v_lshl_add_u64 v[212:213], s[2:3], 0, v[128:129]
	s_mov_b32 m0, s64
	v_lshl_add_u64 v[214:215], s[10:11], 0, v[130:131]
	global_load_lds_dwordx4 v[212:213], off
	v_lshl_add_u64 v[212:213], s[2:3], 0, v[130:131]
	s_add_i32 m0, s64, 0x2000
	s_nop 0
	global_load_lds_dwordx4 v[212:213], off
	v_lshl_add_u64 v[212:213], s[10:11], 0, v[128:129]
	s_mov_b32 m0, s21
	s_nop 0
	global_load_lds_dwordx4 v[212:213], off
	s_mov_b32 m0, s28
	s_nop 0
	global_load_lds_dwordx4 v[214:215], off
	s_waitcnt vmcnt(8)
	s_waitcnt lgkmcnt(0)
	s_barrier
	s_setprio 1
	s_waitcnt lgkmcnt(0)
	v_mfma_f32_16x16x32_bf16 v[60:63], v[146:149], v[178:181], v[60:63]
	v_mfma_f32_16x16x32_bf16 v[56:59], v[154:157], v[178:181], v[56:59]
	v_mfma_f32_16x16x32_bf16 v[44:47], v[146:149], v[186:189], v[44:47]
	v_mfma_f32_16x16x32_bf16 v[40:43], v[154:157], v[186:189], v[40:43]
	v_mfma_f32_16x16x32_bf16 v[28:31], v[146:149], v[194:197], v[28:31]
	v_mfma_f32_16x16x32_bf16 v[24:27], v[154:157], v[194:197], v[24:27]
	v_mfma_f32_16x16x32_bf16 v[12:15], v[146:149], v[202:205], v[12:15]
	v_mfma_f32_16x16x32_bf16 v[8:11], v[154:157], v[202:205], v[8:11]
	v_mfma_f32_16x16x32_bf16 v[60:63], v[150:153], v[182:185], v[60:63]
	v_mfma_f32_16x16x32_bf16 v[56:59], v[158:161], v[182:185], v[56:59]
	v_mfma_f32_16x16x32_bf16 v[44:47], v[150:153], v[190:193], v[44:47]
	v_mfma_f32_16x16x32_bf16 v[40:43], v[158:161], v[190:193], v[40:43]
	v_mfma_f32_16x16x32_bf16 v[28:31], v[150:153], v[198:201], v[28:31]
	v_mfma_f32_16x16x32_bf16 v[24:27], v[158:161], v[198:201], v[24:27]
	v_mfma_f32_16x16x32_bf16 v[12:15], v[150:153], v[206:209], v[12:15]
	v_mfma_f32_16x16x32_bf16 v[8:11], v[158:161], v[206:209], v[8:11]
	s_setprio 0
	s_setprio 1
	v_mfma_f32_16x16x32_bf16 v[52:55], v[162:165], v[178:181], v[52:55]
	v_mfma_f32_16x16x32_bf16 v[48:51], v[170:173], v[178:181], v[48:51]
	v_mfma_f32_16x16x32_bf16 v[36:39], v[162:165], v[186:189], v[36:39]
	v_mfma_f32_16x16x32_bf16 v[32:35], v[170:173], v[186:189], v[32:35]
	v_mfma_f32_16x16x32_bf16 v[20:23], v[162:165], v[194:197], v[20:23]
	v_mfma_f32_16x16x32_bf16 v[16:19], v[170:173], v[194:197], v[16:19]
	v_mfma_f32_16x16x32_bf16 v[4:7], v[162:165], v[202:205], v[4:7]
	v_mfma_f32_16x16x32_bf16 v[0:3], v[170:173], v[202:205], v[0:3]
	v_mfma_f32_16x16x32_bf16 v[52:55], v[166:169], v[182:185], v[52:55]
	v_mfma_f32_16x16x32_bf16 v[48:51], v[174:177], v[182:185], v[48:51]
	v_mfma_f32_16x16x32_bf16 v[36:39], v[166:169], v[190:193], v[36:39]
	v_mfma_f32_16x16x32_bf16 v[32:35], v[174:177], v[190:193], v[32:35]
	v_mfma_f32_16x16x32_bf16 v[20:23], v[166:169], v[198:201], v[20:23]
	v_mfma_f32_16x16x32_bf16 v[16:19], v[174:177], v[198:201], v[16:19]
	v_mfma_f32_16x16x32_bf16 v[4:7], v[166:169], v[206:209], v[4:7]
	v_mfma_f32_16x16x32_bf16 v[0:3], v[174:177], v[206:209], v[0:3]
	s_setprio 0
	s_barrier
	s_add_i32 s64, 0, 0x18000
	s_add_i32 s65, 0, 0x1c000
	v_add_u32_e32 v158, s64, v139
	v_add_u32_e32 v174, s65, v139
	ds_read_b128 v[146:149], v158
	ds_read_b128 v[150:153], v158 offset:1024
	ds_read_b128 v[154:157], v158 offset:2048
	ds_read_b128 v[158:161], v158 offset:3072
	ds_read_b128 v[162:165], v174
	ds_read_b128 v[166:169], v174 offset:1024
	ds_read_b128 v[170:173], v174 offset:2048
	ds_read_b128 v[174:177], v174 offset:3072
	s_add_u32 s2, s10, 0x58000
	s_addc_u32 s3, s11, 0
	s_mov_b32 m0, s29
	v_lshl_add_u64 v[216:217], s[2:3], 0, v[128:129]
	ds_read_b128 v[178:181], v143 offset:32768
	ds_read_b128 v[182:185], v143 offset:33792
	ds_read_b128 v[186:189], v143 offset:34816
	ds_read_b128 v[190:193], v143 offset:35840
	ds_read_b128 v[194:197], v143 offset:36864
	ds_read_b128 v[198:201], v143 offset:37888
	ds_read_b128 v[202:205], v143 offset:38912
	ds_read_b128 v[206:209], v143 offset:39936
	global_load_lds_dwordx4 v[216:217], off
	v_lshl_add_u64 v[216:217], s[2:3], 0, v[130:131]
	s_mov_b32 m0, s34
	s_nop 0
	global_load_lds_dwordx4 v[216:217], off
	s_waitcnt vmcnt(8)
	s_waitcnt lgkmcnt(0)
	s_barrier
	s_setprio 1
	s_waitcnt lgkmcnt(0)
	v_mfma_f32_16x16x32_bf16 v[124:127], v[146:149], v[178:181], v[124:127]
	v_mfma_f32_16x16x32_bf16 v[120:123], v[154:157], v[178:181], v[120:123]
	v_mfma_f32_16x16x32_bf16 v[108:111], v[146:149], v[186:189], v[108:111]
	v_mfma_f32_16x16x32_bf16 v[104:107], v[154:157], v[186:189], v[104:107]
	v_mfma_f32_16x16x32_bf16 v[92:95], v[146:149], v[194:197], v[92:95]
	v_mfma_f32_16x16x32_bf16 v[88:91], v[154:157], v[194:197], v[88:91]
	v_mfma_f32_16x16x32_bf16 v[76:79], v[146:149], v[202:205], v[76:79]
	v_mfma_f32_16x16x32_bf16 v[72:75], v[154:157], v[202:205], v[72:75]
	v_mfma_f32_16x16x32_bf16 v[124:127], v[150:153], v[182:185], v[124:127]
	v_mfma_f32_16x16x32_bf16 v[120:123], v[158:161], v[182:185], v[120:123]
	v_mfma_f32_16x16x32_bf16 v[108:111], v[150:153], v[190:193], v[108:111]
	v_mfma_f32_16x16x32_bf16 v[104:107], v[158:161], v[190:193], v[104:107]
	v_mfma_f32_16x16x32_bf16 v[92:95], v[150:153], v[198:201], v[92:95]
	v_mfma_f32_16x16x32_bf16 v[88:91], v[158:161], v[198:201], v[88:91]
	v_mfma_f32_16x16x32_bf16 v[76:79], v[150:153], v[206:209], v[76:79]
	v_mfma_f32_16x16x32_bf16 v[72:75], v[158:161], v[206:209], v[72:75]
	s_setprio 0
	s_setprio 1
	v_mfma_f32_16x16x32_bf16 v[116:119], v[162:165], v[178:181], v[116:119]
	v_mfma_f32_16x16x32_bf16 v[112:115], v[170:173], v[178:181], v[112:115]
	v_mfma_f32_16x16x32_bf16 v[100:103], v[162:165], v[186:189], v[100:103]
	v_mfma_f32_16x16x32_bf16 v[96:99], v[170:173], v[186:189], v[96:99]
	v_mfma_f32_16x16x32_bf16 v[84:87], v[162:165], v[194:197], v[84:87]
	v_mfma_f32_16x16x32_bf16 v[80:83], v[170:173], v[194:197], v[80:83]
	v_mfma_f32_16x16x32_bf16 v[68:71], v[162:165], v[202:205], v[68:71]
	v_mfma_f32_16x16x32_bf16 v[64:67], v[170:173], v[202:205], v[64:67]
	v_mfma_f32_16x16x32_bf16 v[116:119], v[166:169], v[182:185], v[116:119]
	v_mfma_f32_16x16x32_bf16 v[112:115], v[174:177], v[182:185], v[112:115]
	v_mfma_f32_16x16x32_bf16 v[100:103], v[166:169], v[190:193], v[100:103]
	v_mfma_f32_16x16x32_bf16 v[96:99], v[174:177], v[190:193], v[96:99]
	v_mfma_f32_16x16x32_bf16 v[84:87], v[166:169], v[198:201], v[84:87]
	v_mfma_f32_16x16x32_bf16 v[80:83], v[174:177], v[198:201], v[80:83]
	v_mfma_f32_16x16x32_bf16 v[68:71], v[166:169], v[206:209], v[68:71]
	v_mfma_f32_16x16x32_bf16 v[64:67], v[174:177], v[206:209], v[64:67]
	s_setprio 0
	s_barrier
	s_add_i32 s2, s64, s20
	v_lshl_add_u64 v[136:137], v[136:137], 0, s[8:9]
	s_mov_b32 m0, s2
	ds_read_b128 v[178:181], v143 offset:49152
	ds_read_b128 v[182:185], v143 offset:50176
	ds_read_b128 v[186:189], v143 offset:51200
	ds_read_b128 v[190:193], v143 offset:52224
	ds_read_b128 v[194:197], v143 offset:53248
	ds_read_b128 v[198:201], v143 offset:54272
	ds_read_b128 v[202:205], v143 offset:55296
	ds_read_b128 v[206:209], v143 offset:56320
	global_load_lds_dwordx4 v[136:137], off
	s_add_i32 m0, s2, 0x2000
	s_add_u32 s2, s6, 0x58080
	v_lshl_add_u64 v[136:137], v[210:211], 0, s[8:9]
	s_addc_u32 s3, s7, 0
	s_add_i32 s6, s65, s20
	global_load_lds_dwordx4 v[136:137], off
	v_lshl_add_u64 v[136:137], s[2:3], 0, v[128:129]
	s_mov_b32 m0, s6
	s_nop 0
	global_load_lds_dwordx4 v[136:137], off
	v_lshl_add_u64 v[136:137], s[2:3], 0, v[130:131]
	s_add_i32 m0, s6, 0x2000
	s_nop 0
	global_load_lds_dwordx4 v[136:137], off
	v_lshl_add_u64 v[136:137], v[212:213], 0, s[8:9]
	s_mov_b32 m0, s12
	s_nop 0
	global_load_lds_dwordx4 v[136:137], off
	v_lshl_add_u64 v[136:137], v[214:215], 0, s[8:9]
	s_mov_b32 m0, s13
	s_nop 0
	global_load_lds_dwordx4 v[136:137], off
	s_waitcnt vmcnt(8)
	s_waitcnt lgkmcnt(0)
	s_barrier
	s_setprio 1
	s_waitcnt lgkmcnt(0)
	v_mfma_f32_16x16x32_bf16 v[60:63], v[146:149], v[178:181], v[60:63]
	v_mfma_f32_16x16x32_bf16 v[56:59], v[154:157], v[178:181], v[56:59]
	v_mfma_f32_16x16x32_bf16 v[44:47], v[146:149], v[186:189], v[44:47]
	v_mfma_f32_16x16x32_bf16 v[40:43], v[154:157], v[186:189], v[40:43]
	v_mfma_f32_16x16x32_bf16 v[28:31], v[146:149], v[194:197], v[28:31]
	v_mfma_f32_16x16x32_bf16 v[24:27], v[154:157], v[194:197], v[24:27]
	v_mfma_f32_16x16x32_bf16 v[12:15], v[146:149], v[202:205], v[12:15]
	v_mfma_f32_16x16x32_bf16 v[8:11], v[154:157], v[202:205], v[8:11]
	v_mfma_f32_16x16x32_bf16 v[60:63], v[150:153], v[182:185], v[60:63]
	v_mfma_f32_16x16x32_bf16 v[56:59], v[158:161], v[182:185], v[56:59]
	v_mfma_f32_16x16x32_bf16 v[44:47], v[150:153], v[190:193], v[44:47]
	v_mfma_f32_16x16x32_bf16 v[40:43], v[158:161], v[190:193], v[40:43]
	v_mfma_f32_16x16x32_bf16 v[28:31], v[150:153], v[198:201], v[28:31]
	v_mfma_f32_16x16x32_bf16 v[24:27], v[158:161], v[198:201], v[24:27]
	v_mfma_f32_16x16x32_bf16 v[12:15], v[150:153], v[206:209], v[12:15]
	v_mfma_f32_16x16x32_bf16 v[8:11], v[158:161], v[206:209], v[8:11]
	s_setprio 0
	s_setprio 1
	v_mfma_f32_16x16x32_bf16 v[52:55], v[162:165], v[178:181], v[52:55]
	v_mfma_f32_16x16x32_bf16 v[48:51], v[170:173], v[178:181], v[48:51]
	v_mfma_f32_16x16x32_bf16 v[36:39], v[162:165], v[186:189], v[36:39]
	v_mfma_f32_16x16x32_bf16 v[32:35], v[170:173], v[186:189], v[32:35]
	v_mfma_f32_16x16x32_bf16 v[20:23], v[162:165], v[194:197], v[20:23]
	v_mfma_f32_16x16x32_bf16 v[16:19], v[170:173], v[194:197], v[16:19]
	v_mfma_f32_16x16x32_bf16 v[4:7], v[162:165], v[202:205], v[4:7]
	v_mfma_f32_16x16x32_bf16 v[0:3], v[170:173], v[202:205], v[0:3]
	v_mfma_f32_16x16x32_bf16 v[52:55], v[166:169], v[182:185], v[52:55]
	v_mfma_f32_16x16x32_bf16 v[48:51], v[174:177], v[182:185], v[48:51]
	v_mfma_f32_16x16x32_bf16 v[36:39], v[166:169], v[190:193], v[36:39]
	v_mfma_f32_16x16x32_bf16 v[32:35], v[174:177], v[190:193], v[32:35]
	v_mfma_f32_16x16x32_bf16 v[20:23], v[166:169], v[198:201], v[20:23]
	v_mfma_f32_16x16x32_bf16 v[16:19], v[174:177], v[198:201], v[16:19]
	v_mfma_f32_16x16x32_bf16 v[4:7], v[166:169], v[206:209], v[4:7]
	v_mfma_f32_16x16x32_bf16 v[0:3], v[174:177], v[206:209], v[0:3]
	s_setprio 0
	s_add_i32 s63, s63, 2
	s_add_u32 s61, s61, 0x100
	s_addc_u32 s62, s62, 0
	s_mov_b64 s[2:3], s[4:5]
	s_add_u32 s4, s2, 0x100
	s_addc_u32 s5, s3, 0
	s_cmp_eq_u32 s63, 18
	s_cselect_b32 s11, s53, s5
	s_cselect_b32 s10, s52, s4
	s_cselect_b32 s7, s55, s62
	s_cselect_b32 s6, s54, s61
	s_cmp_gt_u32 s63, 19
	s_barrier
	s_cbranch_scc0 .LBB0_1298
	s_and_b64 vcc, exec, s[48:49]
	s_cbranch_vccz .LBB0_1301
	s_barrier
